# GEMM k-loop micro-edits combined: loop-top scalar block behind LDS reads, redundant lgkmcnt(0) removed, no s_setprio toggling
# speedup vs baseline: 1.0018x; 1.0005x over previous
; #define PG8_AOFF(of, u) do { _Pragma("unroll") for (int hh_ = 0; hh_ < 2; ++hh_) _Pragma("unroll") for (int i_ = 0; i_ < 2; ++i_) { \
;         if constexpr (GATHER) of[hh_][i_] = (unsigned)gidx[(u).pm * 256 + hh_ * 128 + RA[i_]] * (unsigned)(lda * 2) + CA2[i_]; \
;         else of[hh_][i_] = (unsigned)((hh_ * HALF + RA[i_]) * lda) * 2u + CA2[i_]; } } while (0)
; #define PG8_STAGE(bufoff, gbase, voff) do { _Pragma("unroll") for (int _i = 0; _i < 2; ++_i) \
;         __builtin_amdgcn_global_load_lds((const unsigned*)((const char*)(gbase) + (voff)[_i]), (LAS unsigned*)(lds + (bufoff) + ldsw + _i * 8192), 16, 0, 0); } while (0)
; #define PG8_LDA(dst, b, h) do { _Pragma("unroll") for (int m = 0; m < 4; ++m) _Pragma("unroll") for (int k = 0; k < 2; ++k) dst[m][k] = *(const LAS bf16x8*)(lds + PG8_SA(b, h) + aoff + m * 2048 + k * 1024); } while (0)
; #define PG8_LDB(dst, b, h) do { _Pragma("unroll") for (int n = 0; n < 2; ++n) _Pragma("unroll") for (int k = 0; k < 2; ++k) dst[n][k] = *(const LAS bf16x8*)(lds + PG8_SB(b, h) + boff + n * 2048 + k * 1024); } while (0)
; template <class Epi, class Sched, bool GATHER = false>
; __device__ __forceinline__ void gemm_phase(LAS unsigned char* lds, const int lda, const int ldb, const int K, const Sched& S, const Epi& E, const int* gidx = nullptr) {
;     ...
;         for (int t = 0; t < nt; t += 2) {
;             const bool last = (t == nt - 2);
;             if constexpr (GATHER) { if (last && has_next) PG8_AOFF(ofn, nxt); }
;             const char* a1 = cA + (size_t)(t + 1) * kstep;
;             const char* a2 = last ? nA : cA + (size_t)(t + 2) * kstep; const char* b2 = last ? nB : cB + (size_t)(t + 2) * kstep;
;             const char* a3 = a2 + kstep; const char* b3 = b2 + kstep;
;             unsigned o2[2][2];
; #pragma unroll
;             for (int hh = 0; hh < 2; ++hh)
; #pragma unroll
;                 for (int i = 0; i < 2; ++i) { if constexpr (GATHER) o2[hh][i] = last ? ofn[hh][i] : ofc[hh][i]; else o2[hh][i] = ofc[hh][i]; }
;             PG8_LDB(B0, 0, 0); PG8_LDB(B1, 0, 1); PG8_SCHED; PG8_LDA(At, 0, 0); PG8_STAGE(PG8_SA(1, 1), a1, ofc[1]);
;             PG8_WAIT_V(8); PG8_WAIT_L(0); PG8_BAR; PG8_MMA(0, 0, At, B0); PG8_MMA(0, 1, At, B1); PG8_BAR; PG8_SCHED;
;             PG8_LDA(At, 0, 1); PG8_STAGE(PG8_SB(0, 0), b2, voffB); PG8_STAGE(PG8_SB(0, 1), b2 + hstepB, voffB); PG8_STAGE(PG8_SA(0, 0), a2, o2[0]);
.LBB0_428:
	s_add_i32 s28, 0, 0x10000
	s_add_i32 s33, 0, 0x14000
	v_add_u32_e32 v142, s28, v175
	v_add_u32_e32 v158, s33, v175
	ds_read_b128 v[126:129], v142
	ds_read_b128 v[130:133], v142 offset:1024
	ds_read_b128 v[138:141], v142 offset:2048
	ds_read_b128 v[142:145], v142 offset:3072
	ds_read_b128 v[146:149], v158
	ds_read_b128 v[150:153], v158 offset:1024
	ds_read_b128 v[154:157], v158 offset:2048
	ds_read_b128 v[158:161], v158 offset:3072
	v_lshl_add_u64 v[234:235], s[72:73], 0, v[180:181]
	s_add_i32 m0, s59, 0xc000
	ds_read_b128 v[182:185], v229
	ds_read_b128 v[186:189], v229 offset:1024
	ds_read_b128 v[190:193], v229 offset:2048
	ds_read_b128 v[196:199], v229 offset:3072
	ds_read_b128 v[200:203], v229 offset:4096
	ds_read_b128 v[204:207], v229 offset:5120
	ds_read_b128 v[208:211], v229 offset:6144
	ds_read_b128 v[230:233], v229 offset:7168
	s_add_u32 s12, s72, 0x80
	s_addc_u32 s13, s73, 0
	s_cmp_eq_u32 s75, 28
	s_cselect_b32 s67, s81, s13
	s_cselect_b32 s66, s80, s12
	s_cselect_b32 s13, s83, s74
	s_cselect_b32 s12, s82, s60
	global_load_lds_dwordx4 v[234:235], off
	v_lshl_add_u64 v[234:235], s[72:73], 0, v[178:179]
	s_add_i32 m0, s59, 0xe000
	s_nop 0
	global_load_lds_dwordx4 v[234:235], off
	s_waitcnt vmcnt(8)
	s_waitcnt lgkmcnt(0)
	s_barrier
	v_mfma_f32_16x16x32_bf16 v[134:137], v[126:129], v[182:185], v[134:137]
	v_mfma_f32_16x16x32_bf16 v[122:125], v[138:141], v[182:185], v[122:125]
	v_mfma_f32_16x16x32_bf16 v[110:113], v[126:129], v[190:193], v[110:113]
	v_mfma_f32_16x16x32_bf16 v[106:109], v[138:141], v[190:193], v[106:109]
	v_mfma_f32_16x16x32_bf16 v[94:97], v[126:129], v[200:203], v[94:97]
	v_mfma_f32_16x16x32_bf16 v[90:93], v[138:141], v[200:203], v[90:93]
	v_mfma_f32_16x16x32_bf16 v[78:81], v[126:129], v[208:211], v[78:81]
	v_mfma_f32_16x16x32_bf16 v[74:77], v[138:141], v[208:211], v[74:77]
	v_mfma_f32_16x16x32_bf16 v[134:137], v[130:133], v[186:189], v[134:137]
	v_mfma_f32_16x16x32_bf16 v[122:125], v[142:145], v[186:189], v[122:125]
	v_mfma_f32_16x16x32_bf16 v[110:113], v[130:133], v[196:199], v[110:113]
	v_mfma_f32_16x16x32_bf16 v[106:109], v[142:145], v[196:199], v[106:109]
	v_mfma_f32_16x16x32_bf16 v[94:97], v[130:133], v[204:207], v[94:97]
	v_mfma_f32_16x16x32_bf16 v[90:93], v[142:145], v[204:207], v[90:93]
	v_mfma_f32_16x16x32_bf16 v[78:81], v[130:133], v[230:233], v[78:81]
	v_mfma_f32_16x16x32_bf16 v[74:77], v[142:145], v[230:233], v[74:77]
	v_mfma_f32_16x16x32_bf16 v[118:121], v[146:149], v[182:185], v[118:121]
	v_mfma_f32_16x16x32_bf16 v[114:117], v[154:157], v[182:185], v[114:117]
	v_mfma_f32_16x16x32_bf16 v[102:105], v[146:149], v[190:193], v[102:105]
	v_mfma_f32_16x16x32_bf16 v[98:101], v[154:157], v[190:193], v[98:101]
	v_mfma_f32_16x16x32_bf16 v[86:89], v[146:149], v[200:203], v[86:89]
	v_mfma_f32_16x16x32_bf16 v[82:85], v[154:157], v[200:203], v[82:85]
	v_mfma_f32_16x16x32_bf16 v[70:73], v[146:149], v[208:211], v[70:73]
	v_mfma_f32_16x16x32_bf16 v[66:69], v[154:157], v[208:211], v[66:69]
	v_mfma_f32_16x16x32_bf16 v[118:121], v[150:153], v[186:189], v[118:121]
	v_mfma_f32_16x16x32_bf16 v[114:117], v[158:161], v[186:189], v[114:117]
	v_mfma_f32_16x16x32_bf16 v[102:105], v[150:153], v[196:199], v[102:105]
	v_mfma_f32_16x16x32_bf16 v[98:101], v[158:161], v[196:199], v[98:101]
	v_mfma_f32_16x16x32_bf16 v[86:89], v[150:153], v[204:207], v[86:89]
	v_mfma_f32_16x16x32_bf16 v[82:85], v[158:161], v[204:207], v[82:85]
	v_mfma_f32_16x16x32_bf16 v[70:73], v[150:153], v[230:233], v[70:73]
	v_mfma_f32_16x16x32_bf16 v[66:69], v[158:161], v[230:233], v[66:69]
	s_barrier
	s_add_i32 s28, s28, s43
	v_lshl_add_u64 v[234:235], s[12:13], 0, v[162:163]
	s_mov_b32 m0, s28
	ds_read_b128 v[182:185], v229 offset:16384
	ds_read_b128 v[186:189], v229 offset:17408
	ds_read_b128 v[190:193], v229 offset:18432
	ds_read_b128 v[196:199], v229 offset:19456
	ds_read_b128 v[200:203], v229 offset:20480
	ds_read_b128 v[204:207], v229 offset:21504
	ds_read_b128 v[208:211], v229 offset:22528
	ds_read_b128 v[230:233], v229 offset:23552
	global_load_lds_dwordx4 v[234:235], off
	s_add_i32 m0, s28, 0x2000
	s_add_u32 s28, s12, 0x80000
	v_lshl_add_u64 v[236:237], s[12:13], 0, v[164:165]
	s_addc_u32 s29, s13, 0
	s_add_i32 s33, s33, s43
	global_load_lds_dwordx4 v[236:237], off
	v_lshl_add_u64 v[238:239], s[28:29], 0, v[162:163]
	s_mov_b32 m0, s33
	v_lshl_add_u64 v[240:241], s[66:67], 0, v[168:169]
	global_load_lds_dwordx4 v[238:239], off
	v_lshl_add_u64 v[238:239], s[28:29], 0, v[164:165]
	s_add_i32 m0, s33, 0x2000
	s_nop 0
	global_load_lds_dwordx4 v[238:239], off
	v_lshl_add_u64 v[238:239], s[66:67], 0, v[166:167]
	s_mov_b32 m0, s59
	s_nop 0
	global_load_lds_dwordx4 v[238:239], off
	s_mov_b32 m0, s36
	s_nop 0
	global_load_lds_dwordx4 v[240:241], off
	s_waitcnt vmcnt(8)
	s_waitcnt lgkmcnt(0)
	s_barrier
; #define PG8_STAGE(bufoff, gbase, voff) do { _Pragma("unroll") for (int _i = 0; _i < 2; ++_i) \
;         __builtin_amdgcn_global_load_lds((const unsigned*)((const char*)(gbase) + (voff)[_i]), (LAS unsigned*)(lds + (bufoff) + ldsw + _i * 8192), 16, 0, 0); } while (0)
; #define PG8_LDA(dst, b, h) do { _Pragma("unroll") for (int m = 0; m < 4; ++m) _Pragma("unroll") for (int k = 0; k < 2; ++k) dst[m][k] = *(const LAS bf16x8*)(lds + PG8_SA(b, h) + aoff + m * 2048 + k * 1024); } while (0)
; #define PG8_LDB(dst, b, h) do { _Pragma("unroll") for (int n = 0; n < 2; ++n) _Pragma("unroll") for (int k = 0; k < 2; ++k) dst[n][k] = *(const LAS bf16x8*)(lds + PG8_SB(b, h) + boff + n * 2048 + k * 1024); } while (0)
; #define PG8_MMA(ai, bj, At, Bt) do { __builtin_amdgcn_s_setprio(1); _Pragma("unroll") for (int m = 0; m < 4; ++m) _Pragma("unroll") for (int n = 0; n < 2; ++n) _Pragma("unroll") for (int k = 0; k < 2; ++k) \
;         acc[ai][bj][m][n] = __builtin_amdgcn_mfma_f32_16x16x32_bf16(Bt[n][k], At[m][k], acc[ai][bj][m][n], 0, 0, 0); __builtin_amdgcn_s_setprio(0); } while (0)
; #define PG8_WAIT_V(n) asm volatile("s_waitcnt vmcnt(" #n ")" ::: "memory")
; #define PG8_WAIT_L(n) asm volatile("s_waitcnt lgkmcnt(" #n ")" ::: "memory")
; #define PG8_BAR __builtin_amdgcn_s_barrier()
; #define PG8_SCHED __builtin_amdgcn_sched_barrier(0)
; template <class Epi, class Sched, bool GATHER = false>
; __device__ __forceinline__ void gemm_phase(LAS unsigned char* lds, const int lda, const int ldb, const int K, const Sched& S, const Epi& E, const int* gidx = nullptr) {
;     ...
;             PG8_WAIT_V(8); PG8_WAIT_L(0); PG8_BAR; PG8_MMA(1, 0, At, B0); PG8_MMA(1, 1, At, B1); PG8_BAR; PG8_SCHED;
;             PG8_LDB(B0, 1, 0); PG8_LDB(B1, 1, 1); PG8_SCHED; PG8_LDA(At, 1, 0); PG8_STAGE(PG8_SA(0, 1), a2, o2[1]);
;             PG8_WAIT_V(8); PG8_WAIT_L(0); PG8_BAR; PG8_MMA(0, 0, At, B0); PG8_MMA(0, 1, At, B1); PG8_BAR; PG8_SCHED;
	v_mfma_f32_16x16x32_bf16 v[62:65], v[126:129], v[182:185], v[62:65]
	v_mfma_f32_16x16x32_bf16 v[58:61], v[138:141], v[182:185], v[58:61]
	v_mfma_f32_16x16x32_bf16 v[46:49], v[126:129], v[190:193], v[46:49]
	v_mfma_f32_16x16x32_bf16 v[42:45], v[138:141], v[190:193], v[42:45]
	v_mfma_f32_16x16x32_bf16 v[30:33], v[126:129], v[200:203], v[30:33]
	v_mfma_f32_16x16x32_bf16 v[26:29], v[138:141], v[200:203], v[26:29]
	v_mfma_f32_16x16x32_bf16 v[14:17], v[126:129], v[208:211], v[14:17]
	v_mfma_f32_16x16x32_bf16 v[10:13], v[138:141], v[208:211], v[10:13]
	v_mfma_f32_16x16x32_bf16 v[62:65], v[130:133], v[186:189], v[62:65]
	v_mfma_f32_16x16x32_bf16 v[58:61], v[142:145], v[186:189], v[58:61]
	v_mfma_f32_16x16x32_bf16 v[46:49], v[130:133], v[196:199], v[46:49]
	v_mfma_f32_16x16x32_bf16 v[42:45], v[142:145], v[196:199], v[42:45]
	v_mfma_f32_16x16x32_bf16 v[30:33], v[130:133], v[204:207], v[30:33]
	v_mfma_f32_16x16x32_bf16 v[26:29], v[142:145], v[204:207], v[26:29]
	v_mfma_f32_16x16x32_bf16 v[14:17], v[130:133], v[230:233], v[14:17]
	v_mfma_f32_16x16x32_bf16 v[10:13], v[142:145], v[230:233], v[10:13]
	v_mfma_f32_16x16x32_bf16 v[54:57], v[146:149], v[182:185], v[54:57]
	v_mfma_f32_16x16x32_bf16 v[50:53], v[154:157], v[182:185], v[50:53]
	v_mfma_f32_16x16x32_bf16 v[38:41], v[146:149], v[190:193], v[38:41]
	v_mfma_f32_16x16x32_bf16 v[34:37], v[154:157], v[190:193], v[34:37]
	v_mfma_f32_16x16x32_bf16 v[22:25], v[146:149], v[200:203], v[22:25]
	v_mfma_f32_16x16x32_bf16 v[18:21], v[154:157], v[200:203], v[18:21]
	v_mfma_f32_16x16x32_bf16 v[6:9], v[146:149], v[208:211], v[6:9]
	v_mfma_f32_16x16x32_bf16 v[2:5], v[154:157], v[208:211], v[2:5]
	v_mfma_f32_16x16x32_bf16 v[54:57], v[150:153], v[186:189], v[54:57]
	v_mfma_f32_16x16x32_bf16 v[50:53], v[158:161], v[186:189], v[50:53]
	v_mfma_f32_16x16x32_bf16 v[38:41], v[150:153], v[196:199], v[38:41]
	v_mfma_f32_16x16x32_bf16 v[34:37], v[158:161], v[196:199], v[34:37]
	v_mfma_f32_16x16x32_bf16 v[22:25], v[150:153], v[204:207], v[22:25]
	v_mfma_f32_16x16x32_bf16 v[18:21], v[158:161], v[204:207], v[18:21]
	v_mfma_f32_16x16x32_bf16 v[6:9], v[150:153], v[230:233], v[6:9]
	v_mfma_f32_16x16x32_bf16 v[2:5], v[158:161], v[230:233], v[2:5]
	s_barrier
	s_add_i32 s28, 0, 0x18000
	s_add_i32 s29, 0, 0x1c000
	v_add_u32_e32 v142, s28, v175
	v_add_u32_e32 v158, s29, v175
	ds_read_b128 v[126:129], v142
	ds_read_b128 v[130:133], v142 offset:1024
	ds_read_b128 v[138:141], v142 offset:2048
	ds_read_b128 v[142:145], v142 offset:3072
	ds_read_b128 v[146:149], v158
	ds_read_b128 v[150:153], v158 offset:1024
	ds_read_b128 v[154:157], v158 offset:2048
	ds_read_b128 v[158:161], v158 offset:3072
	s_mov_b32 m0, s37
	v_lshl_add_u64 v[242:243], s[66:67], 0, v[170:171]
	ds_read_b128 v[182:185], v229 offset:32768
	ds_read_b128 v[186:189], v229 offset:33792
	ds_read_b128 v[190:193], v229 offset:34816
	ds_read_b128 v[196:199], v229 offset:35840
	ds_read_b128 v[200:203], v229 offset:36864
	ds_read_b128 v[204:207], v229 offset:37888
	ds_read_b128 v[208:211], v229 offset:38912
	ds_read_b128 v[230:233], v229 offset:39936
	global_load_lds_dwordx4 v[242:243], off
	v_lshl_add_u64 v[242:243], s[66:67], 0, v[172:173]
	s_mov_b32 m0, s22
	s_nop 0
	global_load_lds_dwordx4 v[242:243], off
	s_waitcnt vmcnt(8)
	s_waitcnt lgkmcnt(0)
	s_barrier
	v_mfma_f32_16x16x32_bf16 v[134:137], v[126:129], v[182:185], v[134:137]
	v_mfma_f32_16x16x32_bf16 v[122:125], v[138:141], v[182:185], v[122:125]
	v_mfma_f32_16x16x32_bf16 v[110:113], v[126:129], v[190:193], v[110:113]
	v_mfma_f32_16x16x32_bf16 v[106:109], v[138:141], v[190:193], v[106:109]
	v_mfma_f32_16x16x32_bf16 v[94:97], v[126:129], v[200:203], v[94:97]
	v_mfma_f32_16x16x32_bf16 v[90:93], v[138:141], v[200:203], v[90:93]
	v_mfma_f32_16x16x32_bf16 v[78:81], v[126:129], v[208:211], v[78:81]
	v_mfma_f32_16x16x32_bf16 v[74:77], v[138:141], v[208:211], v[74:77]
	v_mfma_f32_16x16x32_bf16 v[134:137], v[130:133], v[186:189], v[134:137]
	v_mfma_f32_16x16x32_bf16 v[122:125], v[142:145], v[186:189], v[122:125]
	v_mfma_f32_16x16x32_bf16 v[110:113], v[130:133], v[196:199], v[110:113]
	v_mfma_f32_16x16x32_bf16 v[106:109], v[142:145], v[196:199], v[106:109]
	v_mfma_f32_16x16x32_bf16 v[94:97], v[130:133], v[204:207], v[94:97]
	v_mfma_f32_16x16x32_bf16 v[90:93], v[142:145], v[204:207], v[90:93]
	v_mfma_f32_16x16x32_bf16 v[78:81], v[130:133], v[230:233], v[78:81]
	v_mfma_f32_16x16x32_bf16 v[74:77], v[142:145], v[230:233], v[74:77]
	v_mfma_f32_16x16x32_bf16 v[118:121], v[146:149], v[182:185], v[118:121]
	v_mfma_f32_16x16x32_bf16 v[114:117], v[154:157], v[182:185], v[114:117]
	v_mfma_f32_16x16x32_bf16 v[102:105], v[146:149], v[190:193], v[102:105]
	v_mfma_f32_16x16x32_bf16 v[98:101], v[154:157], v[190:193], v[98:101]
	v_mfma_f32_16x16x32_bf16 v[86:89], v[146:149], v[200:203], v[86:89]
	v_mfma_f32_16x16x32_bf16 v[82:85], v[154:157], v[200:203], v[82:85]
	v_mfma_f32_16x16x32_bf16 v[70:73], v[146:149], v[208:211], v[70:73]
	v_mfma_f32_16x16x32_bf16 v[66:69], v[154:157], v[208:211], v[66:69]
	v_mfma_f32_16x16x32_bf16 v[118:121], v[150:153], v[186:189], v[118:121]
	v_mfma_f32_16x16x32_bf16 v[114:117], v[158:161], v[186:189], v[114:117]
	v_mfma_f32_16x16x32_bf16 v[102:105], v[150:153], v[196:199], v[102:105]
	v_mfma_f32_16x16x32_bf16 v[98:101], v[158:161], v[196:199], v[98:101]
	v_mfma_f32_16x16x32_bf16 v[86:89], v[150:153], v[204:207], v[86:89]
	v_mfma_f32_16x16x32_bf16 v[82:85], v[158:161], v[204:207], v[82:85]
	v_mfma_f32_16x16x32_bf16 v[70:73], v[150:153], v[230:233], v[70:73]
	v_mfma_f32_16x16x32_bf16 v[66:69], v[158:161], v[230:233], v[66:69]
	s_barrier
; #define PG8_STAGE(bufoff, gbase, voff) do { _Pragma("unroll") for (int _i = 0; _i < 2; ++_i) \
;         __builtin_amdgcn_global_load_lds((const unsigned*)((const char*)(gbase) + (voff)[_i]), (LAS unsigned*)(lds + (bufoff) + ldsw + _i * 8192), 16, 0, 0); } while (0)
; #define PG8_LDA(dst, b, h) do { _Pragma("unroll") for (int m = 0; m < 4; ++m) _Pragma("unroll") for (int k = 0; k < 2; ++k) dst[m][k] = *(const LAS bf16x8*)(lds + PG8_SA(b, h) + aoff + m * 2048 + k * 1024); } while (0)
; #define PG8_MMA(ai, bj, At, Bt) do { __builtin_amdgcn_s_setprio(1); _Pragma("unroll") for (int m = 0; m < 4; ++m) _Pragma("unroll") for (int n = 0; n < 2; ++n) _Pragma("unroll") for (int k = 0; k < 2; ++k) \
;         acc[ai][bj][m][n] = __builtin_amdgcn_mfma_f32_16x16x32_bf16(Bt[n][k], At[m][k], acc[ai][bj][m][n], 0, 0, 0); __builtin_amdgcn_s_setprio(0); } while (0)
; #define PG8_WAIT_V(n) asm volatile("s_waitcnt vmcnt(" #n ")" ::: "memory")
; #define PG8_WAIT_L(n) asm volatile("s_waitcnt lgkmcnt(" #n ")" ::: "memory")
; #define PG8_BAR __builtin_amdgcn_s_barrier()
; #define PG8_SCHED __builtin_amdgcn_sched_barrier(0)
; template <class Epi, class Sched, bool GATHER = false>
; __device__ __forceinline__ void gemm_phase(LAS unsigned char* lds, const int lda, const int ldb, const int K, const Sched& S, const Epi& E, const int* gidx = nullptr) {
;     ...
;             PG8_LDA(At, 1, 1); PG8_STAGE(PG8_SB(1, 0), b3, voffB); PG8_STAGE(PG8_SB(1, 1), b3 + hstepB, voffB); PG8_STAGE(PG8_SA(1, 0), a3, o2[0]);
;             PG8_WAIT_V(8); PG8_WAIT_L(0); PG8_BAR; PG8_MMA(1, 0, At, B0); PG8_MMA(1, 1, At, B1); PG8_BAR; PG8_SCHED;
;         }
;         if (wr == 0) PG8_BAR;
	s_add_i32 s28, s28, s43
	v_lshl_add_u64 v[234:235], v[234:235], 0, s[64:65]
	s_mov_b32 m0, s28
	ds_read_b128 v[182:185], v229 offset:49152
	ds_read_b128 v[186:189], v229 offset:50176
	ds_read_b128 v[190:193], v229 offset:51200
	ds_read_b128 v[196:199], v229 offset:52224
	ds_read_b128 v[200:203], v229 offset:53248
	ds_read_b128 v[204:207], v229 offset:54272
	ds_read_b128 v[208:211], v229 offset:55296
	ds_read_b128 v[230:233], v229 offset:56320
	global_load_lds_dwordx4 v[234:235], off
	s_add_i32 m0, s28, 0x2000
	s_add_u32 s12, s12, 0x80080
	v_lshl_add_u64 v[234:235], v[236:237], 0, s[64:65]
	s_addc_u32 s13, s13, 0
	s_add_i32 s28, s29, s43
	global_load_lds_dwordx4 v[234:235], off
	v_lshl_add_u64 v[234:235], s[12:13], 0, v[162:163]
	s_mov_b32 m0, s28
	s_nop 0
	global_load_lds_dwordx4 v[234:235], off
	v_lshl_add_u64 v[234:235], s[12:13], 0, v[164:165]
	s_add_i32 m0, s28, 0x2000
	s_nop 0
	global_load_lds_dwordx4 v[234:235], off
	v_lshl_add_u64 v[234:235], v[238:239], 0, s[64:65]
	s_mov_b32 m0, s10
	s_nop 0
	global_load_lds_dwordx4 v[234:235], off
	v_lshl_add_u64 v[234:235], v[240:241], 0, s[64:65]
	s_mov_b32 m0, s11
	s_nop 0
	global_load_lds_dwordx4 v[234:235], off
	s_waitcnt vmcnt(8)
	s_waitcnt lgkmcnt(0)
	s_barrier
	v_mfma_f32_16x16x32_bf16 v[62:65], v[126:129], v[182:185], v[62:65]
	v_mfma_f32_16x16x32_bf16 v[58:61], v[138:141], v[182:185], v[58:61]
	v_mfma_f32_16x16x32_bf16 v[46:49], v[126:129], v[190:193], v[46:49]
	v_mfma_f32_16x16x32_bf16 v[42:45], v[138:141], v[190:193], v[42:45]
	v_mfma_f32_16x16x32_bf16 v[30:33], v[126:129], v[200:203], v[30:33]
	v_mfma_f32_16x16x32_bf16 v[26:29], v[138:141], v[200:203], v[26:29]
	v_mfma_f32_16x16x32_bf16 v[14:17], v[126:129], v[208:211], v[14:17]
	v_mfma_f32_16x16x32_bf16 v[10:13], v[138:141], v[208:211], v[10:13]
	v_mfma_f32_16x16x32_bf16 v[62:65], v[130:133], v[186:189], v[62:65]
	v_mfma_f32_16x16x32_bf16 v[58:61], v[142:145], v[186:189], v[58:61]
	v_mfma_f32_16x16x32_bf16 v[46:49], v[130:133], v[196:199], v[46:49]
	v_mfma_f32_16x16x32_bf16 v[42:45], v[142:145], v[196:199], v[42:45]
	v_mfma_f32_16x16x32_bf16 v[30:33], v[130:133], v[204:207], v[30:33]
	v_mfma_f32_16x16x32_bf16 v[26:29], v[142:145], v[204:207], v[26:29]
	v_mfma_f32_16x16x32_bf16 v[14:17], v[130:133], v[230:233], v[14:17]
	v_mfma_f32_16x16x32_bf16 v[10:13], v[142:145], v[230:233], v[10:13]
	v_mfma_f32_16x16x32_bf16 v[54:57], v[146:149], v[182:185], v[54:57]
	v_mfma_f32_16x16x32_bf16 v[50:53], v[154:157], v[182:185], v[50:53]
	v_mfma_f32_16x16x32_bf16 v[38:41], v[146:149], v[190:193], v[38:41]
	v_mfma_f32_16x16x32_bf16 v[34:37], v[154:157], v[190:193], v[34:37]
	v_mfma_f32_16x16x32_bf16 v[22:25], v[146:149], v[200:203], v[22:25]
	v_mfma_f32_16x16x32_bf16 v[18:21], v[154:157], v[200:203], v[18:21]
	v_mfma_f32_16x16x32_bf16 v[6:9], v[146:149], v[208:211], v[6:9]
	v_mfma_f32_16x16x32_bf16 v[2:5], v[154:157], v[208:211], v[2:5]
	v_mfma_f32_16x16x32_bf16 v[54:57], v[150:153], v[186:189], v[54:57]
	v_mfma_f32_16x16x32_bf16 v[50:53], v[158:161], v[186:189], v[50:53]
	v_mfma_f32_16x16x32_bf16 v[38:41], v[150:153], v[196:199], v[38:41]
	v_mfma_f32_16x16x32_bf16 v[34:37], v[158:161], v[196:199], v[34:37]
	v_mfma_f32_16x16x32_bf16 v[22:25], v[150:153], v[204:207], v[22:25]
	v_mfma_f32_16x16x32_bf16 v[18:21], v[158:161], v[204:207], v[18:21]
	v_mfma_f32_16x16x32_bf16 v[6:9], v[150:153], v[230:233], v[6:9]
	v_mfma_f32_16x16x32_bf16 v[2:5], v[158:161], v[230:233], v[2:5]
	s_barrier
	s_add_i32 s75, s75, 2
	s_add_u32 s72, s72, 0x100
	s_addc_u32 s73, s73, 0
	s_add_u32 s60, s60, 0x100
	s_addc_u32 s74, s74, 0
	s_cmp_gt_u32 s75, 29
	s_cbranch_scc0 .LBB0_428
	s_and_b64 vcc, exec, s[48:49]
	s_cbranch_vccz .LBB0_431
	s_barrier

; #define PG8_AOFF(of, u) do { _Pragma("unroll") for (int hh_ = 0; hh_ < 2; ++hh_) _Pragma("unroll") for (int i_ = 0; i_ < 2; ++i_) { \
;         if constexpr (GATHER) of[hh_][i_] = (unsigned)gidx[(u).pm * 256 + hh_ * 128 + RA[i_]] * (unsigned)(lda * 2) + CA2[i_]; \
;         else of[hh_][i_] = (unsigned)((hh_ * HALF + RA[i_]) * lda) * 2u + CA2[i_]; } } while (0)
; #define PG8_STAGE(bufoff, gbase, voff) do { _Pragma("unroll") for (int _i = 0; _i < 2; ++_i) \
;         __builtin_amdgcn_global_load_lds((const unsigned*)((const char*)(gbase) + (voff)[_i]), (LAS unsigned*)(lds + (bufoff) + ldsw + _i * 8192), 16, 0, 0); } while (0)
; #define PG8_LDA(dst, b, h) do { _Pragma("unroll") for (int m = 0; m < 4; ++m) _Pragma("unroll") for (int k = 0; k < 2; ++k) dst[m][k] = *(const LAS bf16x8*)(lds + PG8_SA(b, h) + aoff + m * 2048 + k * 1024); } while (0)
; #define PG8_WAIT_V(n) asm volatile("s_waitcnt vmcnt(" #n ")" ::: "memory")
; #define PG8_WAIT_L(n) asm volatile("s_waitcnt lgkmcnt(" #n ")" ::: "memory")
; template <class Epi, class Sched, bool GATHER = false>
; __device__ __forceinline__ void gemm_phase(LAS unsigned char* lds, const int lda, const int ldb, const int K, const Sched& S, const Epi& E, const int* gidx = nullptr) {
;     ...
;             const bool last = (t == nt - 2);
;             if constexpr (GATHER) { if (last && has_next) PG8_AOFF(ofn, nxt); }
;             const char* a1 = cA + (size_t)(t + 1) * kstep;
;             const char* a2 = last ? nA : cA + (size_t)(t + 2) * kstep; const char* b2 = last ? nB : cB + (size_t)(t + 2) * kstep;
;             const char* a3 = a2 + kstep; const char* b3 = b2 + kstep;
;             unsigned o2[2][2];
; #pragma unroll
;             for (int hh = 0; hh < 2; ++hh)
; #pragma unroll
;                 for (int i = 0; i < 2; ++i) { if constexpr (GATHER) o2[hh][i] = last ? ofn[hh][i] : ofc[hh][i]; else o2[hh][i] = ofc[hh][i]; }
;             PG8_LDB(B0, 0, 0); PG8_LDB(B1, 0, 1); PG8_SCHED; PG8_LDA(At, 0, 0); PG8_STAGE(PG8_SA(1, 1), a1, ofc[1]);
;             PG8_WAIT_V(8); PG8_WAIT_L(0); PG8_BAR; PG8_MMA(0, 0, At, B0); PG8_MMA(0, 1, At, B1); PG8_BAR; PG8_SCHED;
;             PG8_LDA(At, 0, 1); PG8_STAGE(PG8_SB(0, 0), b2, voffB); PG8_STAGE(PG8_SB(0, 1), b2 + hstepB, voffB); PG8_STAGE(PG8_SA(0, 0), a2, o2[0]);
;             PG8_WAIT_V(8); PG8_WAIT_L(0); PG8_BAR; PG8_MMA(1, 0, At, B0); PG8_MMA(1, 1, At, B1); PG8_BAR; PG8_SCHED;
.LBB0_1107:
	s_add_i32 s28, 0, 0x10000
	s_add_i32 s33, 0, 0x14000
	v_add_u32_e32 v86, s28, v178
	v_add_u32_e32 v172, s33, v178
	ds_read_b128 v[70:73], v86
	ds_read_b128 v[78:81], v86 offset:1024
	ds_read_b128 v[82:85], v86 offset:2048
	ds_read_b128 v[86:89], v86 offset:3072
	ds_read_b128 v[146:149], v172
	ds_read_b128 v[150:153], v172 offset:1024
	ds_read_b128 v[168:171], v172 offset:2048
	ds_read_b128 v[172:175], v172 offset:3072
	v_lshl_add_u64 v[176:177], s[34:35], 0, v[166:167]
	s_add_i32 m0, s59, 0xc000
	ds_read_b128 v[182:185], v180
	ds_read_b128 v[186:189], v180 offset:1024
	ds_read_b128 v[190:193], v180 offset:2048
	ds_read_b128 v[196:199], v180 offset:3072
	ds_read_b128 v[200:203], v180 offset:4096
	ds_read_b128 v[204:207], v180 offset:5120
	ds_read_b128 v[208:211], v180 offset:6144
	ds_read_b128 v[228:231], v180 offset:7168
	s_add_u32 s12, s34, 0x80
	s_addc_u32 s13, s35, 0
	s_cmp_eq_u32 s83, 28
	s_cselect_b32 s67, s71, s13
	s_cselect_b32 s66, s70, s12
	s_cselect_b32 s13, s73, s82
	s_cselect_b32 s12, s72, s69
	global_load_lds_dwordx4 v[176:177], off
	v_lshl_add_u64 v[176:177], s[34:35], 0, v[164:165]
	s_add_i32 m0, s59, 0xe000
	s_nop 0
	global_load_lds_dwordx4 v[176:177], off
	s_waitcnt vmcnt(8)
	s_waitcnt lgkmcnt(0)
	s_barrier
	v_mfma_f32_16x16x32_bf16 v[142:145], v[70:73], v[182:185], v[142:145]
	v_mfma_f32_16x16x32_bf16 v[138:141], v[82:85], v[182:185], v[138:141]
	v_mfma_f32_16x16x32_bf16 v[126:129], v[70:73], v[190:193], v[126:129]
	v_mfma_f32_16x16x32_bf16 v[122:125], v[82:85], v[190:193], v[122:125]
	v_mfma_f32_16x16x32_bf16 v[110:113], v[70:73], v[200:203], v[110:113]
	v_mfma_f32_16x16x32_bf16 v[106:109], v[82:85], v[200:203], v[106:109]
	v_mfma_f32_16x16x32_bf16 v[94:97], v[70:73], v[208:211], v[94:97]
	v_mfma_f32_16x16x32_bf16 v[90:93], v[82:85], v[208:211], v[90:93]
	v_mfma_f32_16x16x32_bf16 v[142:145], v[78:81], v[186:189], v[142:145]
	v_mfma_f32_16x16x32_bf16 v[138:141], v[86:89], v[186:189], v[138:141]
	v_mfma_f32_16x16x32_bf16 v[126:129], v[78:81], v[196:199], v[126:129]
	v_mfma_f32_16x16x32_bf16 v[122:125], v[86:89], v[196:199], v[122:125]
	v_mfma_f32_16x16x32_bf16 v[110:113], v[78:81], v[204:207], v[110:113]
	v_mfma_f32_16x16x32_bf16 v[106:109], v[86:89], v[204:207], v[106:109]
	v_mfma_f32_16x16x32_bf16 v[94:97], v[78:81], v[228:231], v[94:97]
	v_mfma_f32_16x16x32_bf16 v[90:93], v[86:89], v[228:231], v[90:93]
	v_mfma_f32_16x16x32_bf16 v[134:137], v[146:149], v[182:185], v[134:137]
	v_mfma_f32_16x16x32_bf16 v[130:133], v[168:171], v[182:185], v[130:133]
	v_mfma_f32_16x16x32_bf16 v[118:121], v[146:149], v[190:193], v[118:121]
	v_mfma_f32_16x16x32_bf16 v[114:117], v[168:171], v[190:193], v[114:117]
	v_mfma_f32_16x16x32_bf16 v[102:105], v[146:149], v[200:203], v[102:105]
	v_mfma_f32_16x16x32_bf16 v[98:101], v[168:171], v[200:203], v[98:101]
	v_mfma_f32_16x16x32_bf16 v[74:77], v[146:149], v[208:211], v[74:77]
	v_mfma_f32_16x16x32_bf16 v[66:69], v[168:171], v[208:211], v[66:69]
	v_mfma_f32_16x16x32_bf16 v[134:137], v[150:153], v[186:189], v[134:137]
	v_mfma_f32_16x16x32_bf16 v[130:133], v[172:175], v[186:189], v[130:133]
	v_mfma_f32_16x16x32_bf16 v[118:121], v[150:153], v[196:199], v[118:121]
	v_mfma_f32_16x16x32_bf16 v[114:117], v[172:175], v[196:199], v[114:117]
	v_mfma_f32_16x16x32_bf16 v[102:105], v[150:153], v[204:207], v[102:105]
	v_mfma_f32_16x16x32_bf16 v[98:101], v[172:175], v[204:207], v[98:101]
	v_mfma_f32_16x16x32_bf16 v[74:77], v[150:153], v[228:231], v[74:77]
	v_mfma_f32_16x16x32_bf16 v[66:69], v[172:175], v[228:231], v[66:69]
	s_barrier
	s_add_i32 s28, s28, s8
	v_lshl_add_u64 v[176:177], s[12:13], 0, v[194:195]
	s_mov_b32 m0, s28
	ds_read_b128 v[182:185], v180 offset:16384
	ds_read_b128 v[186:189], v180 offset:17408
	ds_read_b128 v[190:193], v180 offset:18432
	ds_read_b128 v[196:199], v180 offset:19456
	ds_read_b128 v[200:203], v180 offset:20480
	ds_read_b128 v[204:207], v180 offset:21504
	ds_read_b128 v[208:211], v180 offset:22528
	ds_read_b128 v[228:231], v180 offset:23552
	global_load_lds_dwordx4 v[176:177], off
	s_add_i32 m0, s28, 0x2000
	s_add_u32 s28, s12, 0x80000
	v_lshl_add_u64 v[232:233], s[12:13], 0, v[154:155]
	s_addc_u32 s29, s13, 0
	s_add_i32 s33, s33, s8
	global_load_lds_dwordx4 v[232:233], off
	v_lshl_add_u64 v[234:235], s[28:29], 0, v[194:195]
	s_mov_b32 m0, s33
	v_lshl_add_u64 v[236:237], s[66:67], 0, v[158:159]
	global_load_lds_dwordx4 v[234:235], off
	v_lshl_add_u64 v[234:235], s[28:29], 0, v[154:155]
	s_add_i32 m0, s33, 0x2000
	s_nop 0
	global_load_lds_dwordx4 v[234:235], off
	v_lshl_add_u64 v[234:235], s[66:67], 0, v[156:157]
	s_mov_b32 m0, s59
	s_nop 0
	global_load_lds_dwordx4 v[234:235], off
	s_mov_b32 m0, s60
	s_nop 0
	global_load_lds_dwordx4 v[236:237], off
	s_waitcnt vmcnt(8)
	s_waitcnt lgkmcnt(0)
	s_barrier
; #define PG8_STAGE(bufoff, gbase, voff) do { _Pragma("unroll") for (int _i = 0; _i < 2; ++_i) \
;         __builtin_amdgcn_global_load_lds((const unsigned*)((const char*)(gbase) + (voff)[_i]), (LAS unsigned*)(lds + (bufoff) + ldsw + _i * 8192), 16, 0, 0); } while (0)
; #define PG8_LDA(dst, b, h) do { _Pragma("unroll") for (int m = 0; m < 4; ++m) _Pragma("unroll") for (int k = 0; k < 2; ++k) dst[m][k] = *(const LAS bf16x8*)(lds + PG8_SA(b, h) + aoff + m * 2048 + k * 1024); } while (0)
; #define PG8_LDB(dst, b, h) do { _Pragma("unroll") for (int n = 0; n < 2; ++n) _Pragma("unroll") for (int k = 0; k < 2; ++k) dst[n][k] = *(const LAS bf16x8*)(lds + PG8_SB(b, h) + boff + n * 2048 + k * 1024); } while (0)
; #define PG8_MMA(ai, bj, At, Bt) do { __builtin_amdgcn_s_setprio(1); _Pragma("unroll") for (int m = 0; m < 4; ++m) _Pragma("unroll") for (int n = 0; n < 2; ++n) _Pragma("unroll") for (int k = 0; k < 2; ++k) \
;         acc[ai][bj][m][n] = __builtin_amdgcn_mfma_f32_16x16x32_bf16(Bt[n][k], At[m][k], acc[ai][bj][m][n], 0, 0, 0); __builtin_amdgcn_s_setprio(0); } while (0)
; #define PG8_WAIT_V(n) asm volatile("s_waitcnt vmcnt(" #n ")" ::: "memory")
; #define PG8_WAIT_L(n) asm volatile("s_waitcnt lgkmcnt(" #n ")" ::: "memory")
; #define PG8_BAR __builtin_amdgcn_s_barrier()
; #define PG8_SCHED __builtin_amdgcn_sched_barrier(0)
; template <class Epi, class Sched, bool GATHER = false>
; __device__ __forceinline__ void gemm_phase(LAS unsigned char* lds, const int lda, const int ldb, const int K, const Sched& S, const Epi& E, const int* gidx = nullptr) {
;     ...
;             PG8_WAIT_V(8); PG8_WAIT_L(0); PG8_BAR; PG8_MMA(1, 0, At, B0); PG8_MMA(1, 1, At, B1); PG8_BAR; PG8_SCHED;
;             PG8_LDB(B0, 1, 0); PG8_LDB(B1, 1, 1); PG8_SCHED; PG8_LDA(At, 1, 0); PG8_STAGE(PG8_SA(0, 1), a2, o2[1]);
;             PG8_WAIT_V(8); PG8_WAIT_L(0); PG8_BAR; PG8_MMA(0, 0, At, B0); PG8_MMA(0, 1, At, B1); PG8_BAR; PG8_SCHED;
	v_mfma_f32_16x16x32_bf16 v[62:65], v[70:73], v[182:185], v[62:65]
	v_mfma_f32_16x16x32_bf16 v[58:61], v[82:85], v[182:185], v[58:61]
	v_mfma_f32_16x16x32_bf16 v[46:49], v[70:73], v[190:193], v[46:49]
	v_mfma_f32_16x16x32_bf16 v[38:41], v[82:85], v[190:193], v[38:41]
	v_mfma_f32_16x16x32_bf16 v[26:29], v[70:73], v[200:203], v[26:29]
	v_mfma_f32_16x16x32_bf16 v[18:21], v[82:85], v[200:203], v[18:21]
	v_mfma_f32_16x16x32_bf16 v[6:9], v[70:73], v[208:211], v[6:9]
	v_mfma_f32_16x16x32_bf16 v[2:5], v[82:85], v[208:211], v[2:5]
	v_mfma_f32_16x16x32_bf16 v[62:65], v[78:81], v[186:189], v[62:65]
	v_mfma_f32_16x16x32_bf16 v[58:61], v[86:89], v[186:189], v[58:61]
	v_mfma_f32_16x16x32_bf16 v[46:49], v[78:81], v[196:199], v[46:49]
	v_mfma_f32_16x16x32_bf16 v[38:41], v[86:89], v[196:199], v[38:41]
	v_mfma_f32_16x16x32_bf16 v[26:29], v[78:81], v[204:207], v[26:29]
	v_mfma_f32_16x16x32_bf16 v[18:21], v[86:89], v[204:207], v[18:21]
	v_mfma_f32_16x16x32_bf16 v[6:9], v[78:81], v[228:231], v[6:9]
	v_mfma_f32_16x16x32_bf16 v[2:5], v[86:89], v[228:231], v[2:5]
	v_mfma_f32_16x16x32_bf16 v[54:57], v[146:149], v[182:185], v[54:57]
	v_mfma_f32_16x16x32_bf16 v[50:53], v[168:171], v[182:185], v[50:53]
	v_mfma_f32_16x16x32_bf16 v[42:45], v[146:149], v[190:193], v[42:45]
	v_mfma_f32_16x16x32_bf16 v[34:37], v[168:171], v[190:193], v[34:37]
	v_mfma_f32_16x16x32_bf16 v[30:33], v[146:149], v[200:203], v[30:33]
	v_mfma_f32_16x16x32_bf16 v[22:25], v[168:171], v[200:203], v[22:25]
	v_mfma_f32_16x16x32_bf16 v[14:17], v[146:149], v[208:211], v[14:17]
	v_mfma_f32_16x16x32_bf16 v[10:13], v[168:171], v[208:211], v[10:13]
	v_mfma_f32_16x16x32_bf16 v[54:57], v[150:153], v[186:189], v[54:57]
	v_mfma_f32_16x16x32_bf16 v[50:53], v[172:175], v[186:189], v[50:53]
	v_mfma_f32_16x16x32_bf16 v[42:45], v[150:153], v[196:199], v[42:45]
	v_mfma_f32_16x16x32_bf16 v[34:37], v[172:175], v[196:199], v[34:37]
	v_mfma_f32_16x16x32_bf16 v[30:33], v[150:153], v[204:207], v[30:33]
	v_mfma_f32_16x16x32_bf16 v[22:25], v[172:175], v[204:207], v[22:25]
	v_mfma_f32_16x16x32_bf16 v[14:17], v[150:153], v[228:231], v[14:17]
	v_mfma_f32_16x16x32_bf16 v[10:13], v[172:175], v[228:231], v[10:13]
	s_barrier
	s_add_i32 s28, 0, 0x18000
	s_add_i32 s29, 0, 0x1c000
	v_add_u32_e32 v86, s28, v178
	v_add_u32_e32 v172, s29, v178
	ds_read_b128 v[70:73], v86
	ds_read_b128 v[78:81], v86 offset:1024
	ds_read_b128 v[82:85], v86 offset:2048
	ds_read_b128 v[86:89], v86 offset:3072
	ds_read_b128 v[146:149], v172
	ds_read_b128 v[150:153], v172 offset:1024
	ds_read_b128 v[168:171], v172 offset:2048
	ds_read_b128 v[172:175], v172 offset:3072
	s_mov_b32 m0, s74
	v_lshl_add_u64 v[238:239], s[66:67], 0, v[160:161]
	ds_read_b128 v[182:185], v180 offset:32768
	ds_read_b128 v[186:189], v180 offset:33792
	ds_read_b128 v[190:193], v180 offset:34816
	ds_read_b128 v[196:199], v180 offset:35840
	ds_read_b128 v[200:203], v180 offset:36864
	ds_read_b128 v[204:207], v180 offset:37888
	ds_read_b128 v[208:211], v180 offset:38912
	ds_read_b128 v[228:231], v180 offset:39936
	global_load_lds_dwordx4 v[238:239], off
	v_lshl_add_u64 v[238:239], s[66:67], 0, v[162:163]
	s_mov_b32 m0, s75
	s_nop 0
	global_load_lds_dwordx4 v[238:239], off
	s_waitcnt vmcnt(8)
	s_waitcnt lgkmcnt(0)
	s_barrier
	v_mfma_f32_16x16x32_bf16 v[142:145], v[70:73], v[182:185], v[142:145]
	v_mfma_f32_16x16x32_bf16 v[138:141], v[82:85], v[182:185], v[138:141]
	v_mfma_f32_16x16x32_bf16 v[126:129], v[70:73], v[190:193], v[126:129]
	v_mfma_f32_16x16x32_bf16 v[122:125], v[82:85], v[190:193], v[122:125]
	v_mfma_f32_16x16x32_bf16 v[110:113], v[70:73], v[200:203], v[110:113]
	v_mfma_f32_16x16x32_bf16 v[106:109], v[82:85], v[200:203], v[106:109]
	v_mfma_f32_16x16x32_bf16 v[94:97], v[70:73], v[208:211], v[94:97]
	v_mfma_f32_16x16x32_bf16 v[90:93], v[82:85], v[208:211], v[90:93]
	v_mfma_f32_16x16x32_bf16 v[142:145], v[78:81], v[186:189], v[142:145]
	v_mfma_f32_16x16x32_bf16 v[138:141], v[86:89], v[186:189], v[138:141]
	v_mfma_f32_16x16x32_bf16 v[126:129], v[78:81], v[196:199], v[126:129]
	v_mfma_f32_16x16x32_bf16 v[122:125], v[86:89], v[196:199], v[122:125]
	v_mfma_f32_16x16x32_bf16 v[110:113], v[78:81], v[204:207], v[110:113]
	v_mfma_f32_16x16x32_bf16 v[106:109], v[86:89], v[204:207], v[106:109]
	v_mfma_f32_16x16x32_bf16 v[94:97], v[78:81], v[228:231], v[94:97]
	v_mfma_f32_16x16x32_bf16 v[90:93], v[86:89], v[228:231], v[90:93]
	v_mfma_f32_16x16x32_bf16 v[134:137], v[146:149], v[182:185], v[134:137]
	v_mfma_f32_16x16x32_bf16 v[130:133], v[168:171], v[182:185], v[130:133]
	v_mfma_f32_16x16x32_bf16 v[118:121], v[146:149], v[190:193], v[118:121]
	v_mfma_f32_16x16x32_bf16 v[114:117], v[168:171], v[190:193], v[114:117]
	v_mfma_f32_16x16x32_bf16 v[102:105], v[146:149], v[200:203], v[102:105]
	v_mfma_f32_16x16x32_bf16 v[98:101], v[168:171], v[200:203], v[98:101]
	v_mfma_f32_16x16x32_bf16 v[74:77], v[146:149], v[208:211], v[74:77]
	v_mfma_f32_16x16x32_bf16 v[66:69], v[168:171], v[208:211], v[66:69]
	v_mfma_f32_16x16x32_bf16 v[134:137], v[150:153], v[186:189], v[134:137]
	v_mfma_f32_16x16x32_bf16 v[130:133], v[172:175], v[186:189], v[130:133]
	v_mfma_f32_16x16x32_bf16 v[118:121], v[150:153], v[196:199], v[118:121]
	v_mfma_f32_16x16x32_bf16 v[114:117], v[172:175], v[196:199], v[114:117]
	v_mfma_f32_16x16x32_bf16 v[102:105], v[150:153], v[204:207], v[102:105]
	v_mfma_f32_16x16x32_bf16 v[98:101], v[172:175], v[204:207], v[98:101]
	v_mfma_f32_16x16x32_bf16 v[74:77], v[150:153], v[228:231], v[74:77]
	v_mfma_f32_16x16x32_bf16 v[66:69], v[172:175], v[228:231], v[66:69]
	s_barrier
; #define PG8_STAGE(bufoff, gbase, voff) do { _Pragma("unroll") for (int _i = 0; _i < 2; ++_i) \
;         __builtin_amdgcn_global_load_lds((const unsigned*)((const char*)(gbase) + (voff)[_i]), (LAS unsigned*)(lds + (bufoff) + ldsw + _i * 8192), 16, 0, 0); } while (0)
; #define PG8_LDA(dst, b, h) do { _Pragma("unroll") for (int m = 0; m < 4; ++m) _Pragma("unroll") for (int k = 0; k < 2; ++k) dst[m][k] = *(const LAS bf16x8*)(lds + PG8_SA(b, h) + aoff + m * 2048 + k * 1024); } while (0)
; #define PG8_MMA(ai, bj, At, Bt) do { __builtin_amdgcn_s_setprio(1); _Pragma("unroll") for (int m = 0; m < 4; ++m) _Pragma("unroll") for (int n = 0; n < 2; ++n) _Pragma("unroll") for (int k = 0; k < 2; ++k) \
;         acc[ai][bj][m][n] = __builtin_amdgcn_mfma_f32_16x16x32_bf16(Bt[n][k], At[m][k], acc[ai][bj][m][n], 0, 0, 0); __builtin_amdgcn_s_setprio(0); } while (0)
; #define PG8_WAIT_V(n) asm volatile("s_waitcnt vmcnt(" #n ")" ::: "memory")
; #define PG8_WAIT_L(n) asm volatile("s_waitcnt lgkmcnt(" #n ")" ::: "memory")
; #define PG8_BAR __builtin_amdgcn_s_barrier()
; #define PG8_SCHED __builtin_amdgcn_sched_barrier(0)
; template <class Epi, class Sched, bool GATHER = false>
; __device__ __forceinline__ void gemm_phase(LAS unsigned char* lds, const int lda, const int ldb, const int K, const Sched& S, const Epi& E, const int* gidx = nullptr) {
;     ...
;             PG8_LDA(At, 1, 1); PG8_STAGE(PG8_SB(1, 0), b3, voffB); PG8_STAGE(PG8_SB(1, 1), b3 + hstepB, voffB); PG8_STAGE(PG8_SA(1, 0), a3, o2[0]);
;             PG8_WAIT_V(8); PG8_WAIT_L(0); PG8_BAR; PG8_MMA(1, 0, At, B0); PG8_MMA(1, 1, At, B1); PG8_BAR; PG8_SCHED;
;         }
;         if (wr == 0) PG8_BAR;
	s_add_i32 s28, s28, s8
	v_lshl_add_u64 v[176:177], v[176:177], 0, s[64:65]
	s_mov_b32 m0, s28
	ds_read_b128 v[182:185], v180 offset:49152
	ds_read_b128 v[186:189], v180 offset:50176
	ds_read_b128 v[190:193], v180 offset:51200
	ds_read_b128 v[196:199], v180 offset:52224
	ds_read_b128 v[200:203], v180 offset:53248
	ds_read_b128 v[204:207], v180 offset:54272
	ds_read_b128 v[208:211], v180 offset:55296
	ds_read_b128 v[228:231], v180 offset:56320
	global_load_lds_dwordx4 v[176:177], off
	s_add_i32 m0, s28, 0x2000
	s_add_u32 s12, s12, 0x80080
	v_lshl_add_u64 v[176:177], v[232:233], 0, s[64:65]
	s_addc_u32 s13, s13, 0
	s_add_i32 s28, s29, s8
	global_load_lds_dwordx4 v[176:177], off
	v_lshl_add_u64 v[176:177], s[12:13], 0, v[194:195]
	s_mov_b32 m0, s28
	s_nop 0
	global_load_lds_dwordx4 v[176:177], off
	v_lshl_add_u64 v[176:177], s[12:13], 0, v[154:155]
	s_add_i32 m0, s28, 0x2000
	s_nop 0
	global_load_lds_dwordx4 v[176:177], off
	v_lshl_add_u64 v[176:177], v[234:235], 0, s[64:65]
	s_mov_b32 m0, s76
	s_nop 0
	global_load_lds_dwordx4 v[176:177], off
	v_lshl_add_u64 v[176:177], v[236:237], 0, s[64:65]
	s_mov_b32 m0, s77
	s_nop 0
	global_load_lds_dwordx4 v[176:177], off
	s_waitcnt vmcnt(8)
	s_waitcnt lgkmcnt(0)
	s_barrier
	v_mfma_f32_16x16x32_bf16 v[62:65], v[70:73], v[182:185], v[62:65]
	v_mfma_f32_16x16x32_bf16 v[58:61], v[82:85], v[182:185], v[58:61]
	v_mfma_f32_16x16x32_bf16 v[46:49], v[70:73], v[190:193], v[46:49]
	v_mfma_f32_16x16x32_bf16 v[38:41], v[82:85], v[190:193], v[38:41]
	v_mfma_f32_16x16x32_bf16 v[26:29], v[70:73], v[200:203], v[26:29]
	v_mfma_f32_16x16x32_bf16 v[18:21], v[82:85], v[200:203], v[18:21]
	v_mfma_f32_16x16x32_bf16 v[6:9], v[70:73], v[208:211], v[6:9]
	v_mfma_f32_16x16x32_bf16 v[2:5], v[82:85], v[208:211], v[2:5]
	v_mfma_f32_16x16x32_bf16 v[62:65], v[78:81], v[186:189], v[62:65]
	v_mfma_f32_16x16x32_bf16 v[58:61], v[86:89], v[186:189], v[58:61]
	v_mfma_f32_16x16x32_bf16 v[46:49], v[78:81], v[196:199], v[46:49]
	v_mfma_f32_16x16x32_bf16 v[38:41], v[86:89], v[196:199], v[38:41]
	v_mfma_f32_16x16x32_bf16 v[26:29], v[78:81], v[204:207], v[26:29]
	v_mfma_f32_16x16x32_bf16 v[18:21], v[86:89], v[204:207], v[18:21]
	v_mfma_f32_16x16x32_bf16 v[6:9], v[78:81], v[228:231], v[6:9]
	v_mfma_f32_16x16x32_bf16 v[2:5], v[86:89], v[228:231], v[2:5]
	v_mfma_f32_16x16x32_bf16 v[54:57], v[146:149], v[182:185], v[54:57]
	v_mfma_f32_16x16x32_bf16 v[50:53], v[168:171], v[182:185], v[50:53]
	v_mfma_f32_16x16x32_bf16 v[42:45], v[146:149], v[190:193], v[42:45]
	v_mfma_f32_16x16x32_bf16 v[34:37], v[168:171], v[190:193], v[34:37]
	v_mfma_f32_16x16x32_bf16 v[30:33], v[146:149], v[200:203], v[30:33]
	v_mfma_f32_16x16x32_bf16 v[22:25], v[168:171], v[200:203], v[22:25]
	v_mfma_f32_16x16x32_bf16 v[14:17], v[146:149], v[208:211], v[14:17]
	v_mfma_f32_16x16x32_bf16 v[10:13], v[168:171], v[208:211], v[10:13]
	v_mfma_f32_16x16x32_bf16 v[54:57], v[150:153], v[186:189], v[54:57]
	v_mfma_f32_16x16x32_bf16 v[50:53], v[172:175], v[186:189], v[50:53]
	v_mfma_f32_16x16x32_bf16 v[42:45], v[150:153], v[196:199], v[42:45]
	v_mfma_f32_16x16x32_bf16 v[34:37], v[172:175], v[196:199], v[34:37]
	v_mfma_f32_16x16x32_bf16 v[30:33], v[150:153], v[204:207], v[30:33]
	v_mfma_f32_16x16x32_bf16 v[22:25], v[172:175], v[204:207], v[22:25]
	v_mfma_f32_16x16x32_bf16 v[14:17], v[150:153], v[228:231], v[14:17]
	v_mfma_f32_16x16x32_bf16 v[10:13], v[172:175], v[228:231], v[10:13]
	s_barrier
	s_add_i32 s83, s83, 2
	s_add_u32 s34, s34, 0x100
	s_addc_u32 s35, s35, 0
	s_add_u32 s69, s69, 0x100
	s_addc_u32 s82, s82, 0
	s_cmp_gt_u32 s83, 29
	s_cbranch_scc0 .LBB0_1107
	s_and_b64 vcc, exec, s[48:49]
	s_cbranch_vccz .LBB0_1110
	s_barrier

; #define PG8_AOFF(of, u) do { _Pragma("unroll") for (int hh_ = 0; hh_ < 2; ++hh_) _Pragma("unroll") for (int i_ = 0; i_ < 2; ++i_) { \
;         if constexpr (GATHER) of[hh_][i_] = (unsigned)gidx[(u).pm * 256 + hh_ * 128 + RA[i_]] * (unsigned)(lda * 2) + CA2[i_]; \
;         else of[hh_][i_] = (unsigned)((hh_ * HALF + RA[i_]) * lda) * 2u + CA2[i_]; } } while (0)
; #define PG8_STAGE(bufoff, gbase, voff) do { _Pragma("unroll") for (int _i = 0; _i < 2; ++_i) \
;         __builtin_amdgcn_global_load_lds((const unsigned*)((const char*)(gbase) + (voff)[_i]), (LAS unsigned*)(lds + (bufoff) + ldsw + _i * 8192), 16, 0, 0); } while (0)
; #define PG8_LDA(dst, b, h) do { _Pragma("unroll") for (int m = 0; m < 4; ++m) _Pragma("unroll") for (int k = 0; k < 2; ++k) dst[m][k] = *(const LAS bf16x8*)(lds + PG8_SA(b, h) + aoff + m * 2048 + k * 1024); } while (0)
; #define PG8_WAIT_V(n) asm volatile("s_waitcnt vmcnt(" #n ")" ::: "memory")
; #define PG8_WAIT_L(n) asm volatile("s_waitcnt lgkmcnt(" #n ")" ::: "memory")
; template <class Epi, class Sched, bool GATHER = false>
; __device__ __forceinline__ void gemm_phase(LAS unsigned char* lds, const int lda, const int ldb, const int K, const Sched& S, const Epi& E, const int* gidx = nullptr) {
;     ...
;             const bool last = (t == nt - 2);
;             if constexpr (GATHER) { if (last && has_next) PG8_AOFF(ofn, nxt); }
;             const char* a1 = cA + (size_t)(t + 1) * kstep;
;             const char* a2 = last ? nA : cA + (size_t)(t + 2) * kstep; const char* b2 = last ? nB : cB + (size_t)(t + 2) * kstep;
;             const char* a3 = a2 + kstep; const char* b3 = b2 + kstep;
;             unsigned o2[2][2];
; #pragma unroll
;             for (int hh = 0; hh < 2; ++hh)
; #pragma unroll
;                 for (int i = 0; i < 2; ++i) { if constexpr (GATHER) o2[hh][i] = last ? ofn[hh][i] : ofc[hh][i]; else o2[hh][i] = ofc[hh][i]; }
;             PG8_LDB(B0, 0, 0); PG8_LDB(B1, 0, 1); PG8_SCHED; PG8_LDA(At, 0, 0); PG8_STAGE(PG8_SA(1, 1), a1, ofc[1]);
;             PG8_WAIT_V(8); PG8_WAIT_L(0); PG8_BAR; PG8_MMA(0, 0, At, B0); PG8_MMA(0, 1, At, B1); PG8_BAR; PG8_SCHED;
;             PG8_LDA(At, 0, 1); PG8_STAGE(PG8_SB(0, 0), b2, voffB); PG8_STAGE(PG8_SB(0, 1), b2 + hstepB, voffB); PG8_STAGE(PG8_SA(0, 0), a2, o2[0]);
;             PG8_WAIT_V(8); PG8_WAIT_L(0); PG8_BAR; PG8_MMA(1, 0, At, B0); PG8_MMA(1, 1, At, B1); PG8_BAR; PG8_SCHED;
.LBB0_1186:
	s_add_i32 s28, 0, 0x10000
	s_add_i32 s33, 0, 0x14000
	v_add_u32_e32 v102, s28, v84
	v_add_u32_e32 v118, s33, v84
	ds_read_b128 v[90:93], v102
	ds_read_b128 v[94:97], v102 offset:1024
	ds_read_b128 v[98:101], v102 offset:2048
	ds_read_b128 v[102:105], v102 offset:3072
	ds_read_b128 v[106:109], v118
	ds_read_b128 v[110:113], v118 offset:1024
	ds_read_b128 v[114:117], v118 offset:2048
	ds_read_b128 v[118:121], v118 offset:3072
	v_lshl_add_u64 v[204:205], v[82:83], 0, s[12:13]
	s_add_i32 m0, s51, 0xc000
	ds_read_b128 v[130:133], v85
	ds_read_b128 v[134:137], v85 offset:1024
	ds_read_b128 v[186:189], v85 offset:2048
	ds_read_b128 v[190:193], v85 offset:3072
	ds_read_b128 v[196:199], v85 offset:4096
	ds_read_b128 v[200:203], v85 offset:5120
	ds_read_b128 v[208:211], v85 offset:6144
	ds_read_b128 v[228:231], v85 offset:7168
	s_add_u32 s28, s74, s12
	s_addc_u32 s29, s75, s13
	s_add_u32 s28, s28, 0x100
	s_addc_u32 s29, s29, 0
	s_add_u32 s33, s68, s12
	s_addc_u32 s34, s69, s13
	s_cmpk_eq_i32 s12, 0xf00
	s_cselect_b32 s49, s75, s29
	s_cselect_b32 s48, s74, s28
	s_cselect_b32 s35, s45, s34
	s_cselect_b32 s34, s44, s33
	s_add_i32 s28, 0, 0x10000
	s_add_i32 s33, 0, 0x14000
	global_load_lds_dwordx4 v[204:205], off
	v_lshl_add_u64 v[204:205], v[80:81], 0, s[12:13]
	s_add_i32 m0, s51, 0xe000
	s_nop 0
	global_load_lds_dwordx4 v[204:205], off
	s_waitcnt vmcnt(8)
	s_waitcnt lgkmcnt(0)
	s_barrier
	v_mfma_f32_16x16x32_bf16 v[182:185], v[90:93], v[130:133], v[182:185]
	v_mfma_f32_16x16x32_bf16 v[178:181], v[98:101], v[130:133], v[178:181]
	v_mfma_f32_16x16x32_bf16 v[166:169], v[90:93], v[186:189], v[166:169]
	v_mfma_f32_16x16x32_bf16 v[162:165], v[98:101], v[186:189], v[162:165]
	v_mfma_f32_16x16x32_bf16 v[150:153], v[90:93], v[196:199], v[150:153]
	v_mfma_f32_16x16x32_bf16 v[146:149], v[98:101], v[196:199], v[146:149]
	v_mfma_f32_16x16x32_bf16 v[126:129], v[90:93], v[208:211], v[126:129]
	v_mfma_f32_16x16x32_bf16 v[122:125], v[98:101], v[208:211], v[122:125]
	v_mfma_f32_16x16x32_bf16 v[182:185], v[94:97], v[134:137], v[182:185]
	v_mfma_f32_16x16x32_bf16 v[178:181], v[102:105], v[134:137], v[178:181]
	v_mfma_f32_16x16x32_bf16 v[166:169], v[94:97], v[190:193], v[166:169]
	v_mfma_f32_16x16x32_bf16 v[162:165], v[102:105], v[190:193], v[162:165]
	v_mfma_f32_16x16x32_bf16 v[150:153], v[94:97], v[200:203], v[150:153]
	v_mfma_f32_16x16x32_bf16 v[146:149], v[102:105], v[200:203], v[146:149]
	v_mfma_f32_16x16x32_bf16 v[126:129], v[94:97], v[228:231], v[126:129]
	v_mfma_f32_16x16x32_bf16 v[122:125], v[102:105], v[228:231], v[122:125]
	v_mfma_f32_16x16x32_bf16 v[174:177], v[106:109], v[130:133], v[174:177]
	v_mfma_f32_16x16x32_bf16 v[130:133], v[114:117], v[130:133], v[170:173]
	v_mfma_f32_16x16x32_bf16 v[154:157], v[114:117], v[186:189], v[154:157]
	v_mfma_f32_16x16x32_bf16 v[142:145], v[106:109], v[196:199], v[142:145]
	v_mfma_f32_16x16x32_bf16 v[138:141], v[114:117], v[196:199], v[138:141]
	v_mfma_f32_16x16x32_bf16 v[86:89], v[106:109], v[208:211], v[86:89]
	v_mfma_f32_16x16x32_bf16 v[74:77], v[114:117], v[208:211], v[74:77]
	v_mfma_f32_16x16x32_bf16 v[174:177], v[110:113], v[134:137], v[174:177]
	v_mfma_f32_16x16x32_bf16 v[130:133], v[118:121], v[134:137], v[130:133]
	v_mfma_f32_16x16x32_bf16 v[134:137], v[106:109], v[186:189], v[158:161]
	v_mfma_f32_16x16x32_bf16 v[154:157], v[118:121], v[190:193], v[154:157]
	v_mfma_f32_16x16x32_bf16 v[142:145], v[110:113], v[200:203], v[142:145]
	v_mfma_f32_16x16x32_bf16 v[138:141], v[118:121], v[200:203], v[138:141]
	v_mfma_f32_16x16x32_bf16 v[86:89], v[110:113], v[228:231], v[86:89]
	v_mfma_f32_16x16x32_bf16 v[74:77], v[118:121], v[228:231], v[74:77]
	v_mfma_f32_16x16x32_bf16 v[134:137], v[110:113], v[190:193], v[134:137]
	s_barrier
	s_add_i32 s28, s28, s50
	v_lshl_add_u64 v[204:205], s[34:35], 0, v[194:195]
	s_mov_b32 m0, s28
	ds_read_b128 v[158:161], v85 offset:16384
	ds_read_b128 v[170:173], v85 offset:17408
	ds_read_b128 v[186:189], v85 offset:18432
	ds_read_b128 v[190:193], v85 offset:19456
	ds_read_b128 v[196:199], v85 offset:20480
	ds_read_b128 v[200:203], v85 offset:21504
	ds_read_b128 v[208:211], v85 offset:22528
	ds_read_b128 v[228:231], v85 offset:23552
	global_load_lds_dwordx4 v[204:205], off
	s_add_i32 m0, s28, 0x2000
	s_add_u32 s28, s34, 0x80000
	v_lshl_add_u64 v[232:233], s[34:35], 0, v[2:3]
	s_addc_u32 s29, s35, 0
	s_add_i32 s33, s33, s50
	global_load_lds_dwordx4 v[232:233], off
	v_lshl_add_u64 v[234:235], s[28:29], 0, v[194:195]
	s_mov_b32 m0, s33
	v_lshl_add_u64 v[236:237], s[48:49], 0, v[6:7]
	global_load_lds_dwordx4 v[234:235], off
	v_lshl_add_u64 v[234:235], s[28:29], 0, v[2:3]
	s_add_i32 m0, s33, 0x2000
	s_nop 0
	global_load_lds_dwordx4 v[234:235], off
	v_lshl_add_u64 v[234:235], s[48:49], 0, v[4:5]
	s_mov_b32 m0, s51
	s_nop 0
	global_load_lds_dwordx4 v[234:235], off
	s_mov_b32 m0, s60
	s_nop 0
	global_load_lds_dwordx4 v[236:237], off
	s_waitcnt vmcnt(8)
	s_waitcnt lgkmcnt(0)
	s_barrier
; #define PG8_STAGE(bufoff, gbase, voff) do { _Pragma("unroll") for (int _i = 0; _i < 2; ++_i) \
;         __builtin_amdgcn_global_load_lds((const unsigned*)((const char*)(gbase) + (voff)[_i]), (LAS unsigned*)(lds + (bufoff) + ldsw + _i * 8192), 16, 0, 0); } while (0)
; #define PG8_LDA(dst, b, h) do { _Pragma("unroll") for (int m = 0; m < 4; ++m) _Pragma("unroll") for (int k = 0; k < 2; ++k) dst[m][k] = *(const LAS bf16x8*)(lds + PG8_SA(b, h) + aoff + m * 2048 + k * 1024); } while (0)
; #define PG8_LDB(dst, b, h) do { _Pragma("unroll") for (int n = 0; n < 2; ++n) _Pragma("unroll") for (int k = 0; k < 2; ++k) dst[n][k] = *(const LAS bf16x8*)(lds + PG8_SB(b, h) + boff + n * 2048 + k * 1024); } while (0)
; #define PG8_MMA(ai, bj, At, Bt) do { __builtin_amdgcn_s_setprio(1); _Pragma("unroll") for (int m = 0; m < 4; ++m) _Pragma("unroll") for (int n = 0; n < 2; ++n) _Pragma("unroll") for (int k = 0; k < 2; ++k) \
;         acc[ai][bj][m][n] = __builtin_amdgcn_mfma_f32_16x16x32_bf16(Bt[n][k], At[m][k], acc[ai][bj][m][n], 0, 0, 0); __builtin_amdgcn_s_setprio(0); } while (0)
; #define PG8_WAIT_V(n) asm volatile("s_waitcnt vmcnt(" #n ")" ::: "memory")
; #define PG8_WAIT_L(n) asm volatile("s_waitcnt lgkmcnt(" #n ")" ::: "memory")
; #define PG8_BAR __builtin_amdgcn_s_barrier()
; #define PG8_SCHED __builtin_amdgcn_sched_barrier(0)
; template <class Epi, class Sched, bool GATHER = false>
; __device__ __forceinline__ void gemm_phase(LAS unsigned char* lds, const int lda, const int ldb, const int K, const Sched& S, const Epi& E, const int* gidx = nullptr) {
;     ...
;             PG8_WAIT_V(8); PG8_WAIT_L(0); PG8_BAR; PG8_MMA(1, 0, At, B0); PG8_MMA(1, 1, At, B1); PG8_BAR; PG8_SCHED;
;             PG8_LDB(B0, 1, 0); PG8_LDB(B1, 1, 1); PG8_SCHED; PG8_LDA(At, 1, 0); PG8_STAGE(PG8_SA(0, 1), a2, o2[1]);
;             PG8_WAIT_V(8); PG8_WAIT_L(0); PG8_BAR; PG8_MMA(0, 0, At, B0); PG8_MMA(0, 1, At, B1); PG8_BAR; PG8_SCHED;
	v_mfma_f32_16x16x32_bf16 v[70:73], v[90:93], v[158:161], v[70:73]
	v_mfma_f32_16x16x32_bf16 v[66:69], v[98:101], v[158:161], v[66:69]
	v_mfma_f32_16x16x32_bf16 v[54:57], v[90:93], v[186:189], v[54:57]
	v_mfma_f32_16x16x32_bf16 v[46:49], v[98:101], v[186:189], v[46:49]
	v_mfma_f32_16x16x32_bf16 v[34:37], v[90:93], v[196:199], v[34:37]
	v_mfma_f32_16x16x32_bf16 v[26:29], v[98:101], v[196:199], v[26:29]
	v_mfma_f32_16x16x32_bf16 v[22:25], v[90:93], v[208:211], v[22:25]
	v_mfma_f32_16x16x32_bf16 v[18:21], v[98:101], v[208:211], v[18:21]
	v_mfma_f32_16x16x32_bf16 v[70:73], v[94:97], v[170:173], v[70:73]
	v_mfma_f32_16x16x32_bf16 v[66:69], v[102:105], v[170:173], v[66:69]
	v_mfma_f32_16x16x32_bf16 v[54:57], v[94:97], v[190:193], v[54:57]
	v_mfma_f32_16x16x32_bf16 v[46:49], v[102:105], v[190:193], v[46:49]
	v_mfma_f32_16x16x32_bf16 v[34:37], v[94:97], v[200:203], v[34:37]
	v_mfma_f32_16x16x32_bf16 v[26:29], v[102:105], v[200:203], v[26:29]
	v_mfma_f32_16x16x32_bf16 v[22:25], v[94:97], v[228:231], v[22:25]
	v_mfma_f32_16x16x32_bf16 v[18:21], v[102:105], v[228:231], v[18:21]
	v_mfma_f32_16x16x32_bf16 v[62:65], v[106:109], v[158:161], v[62:65]
	v_mfma_f32_16x16x32_bf16 v[58:61], v[114:117], v[158:161], v[58:61]
	v_mfma_f32_16x16x32_bf16 v[50:53], v[106:109], v[186:189], v[50:53]
	v_mfma_f32_16x16x32_bf16 v[42:45], v[114:117], v[186:189], v[42:45]
	v_mfma_f32_16x16x32_bf16 v[38:41], v[106:109], v[196:199], v[38:41]
	v_mfma_f32_16x16x32_bf16 v[30:33], v[114:117], v[196:199], v[30:33]
	v_mfma_f32_16x16x32_bf16 v[14:17], v[106:109], v[208:211], v[14:17]
	v_mfma_f32_16x16x32_bf16 v[10:13], v[114:117], v[208:211], v[10:13]
	v_mfma_f32_16x16x32_bf16 v[62:65], v[110:113], v[170:173], v[62:65]
	v_mfma_f32_16x16x32_bf16 v[58:61], v[118:121], v[170:173], v[58:61]
	v_mfma_f32_16x16x32_bf16 v[50:53], v[110:113], v[190:193], v[50:53]
	v_mfma_f32_16x16x32_bf16 v[42:45], v[118:121], v[190:193], v[42:45]
	v_mfma_f32_16x16x32_bf16 v[38:41], v[110:113], v[200:203], v[38:41]
	v_mfma_f32_16x16x32_bf16 v[30:33], v[118:121], v[200:203], v[30:33]
	v_mfma_f32_16x16x32_bf16 v[14:17], v[110:113], v[228:231], v[14:17]
	v_mfma_f32_16x16x32_bf16 v[10:13], v[118:121], v[228:231], v[10:13]
	s_barrier
	s_add_i32 s28, 0, 0x18000
	s_add_i32 s33, 0, 0x1c000
	v_add_u32_e32 v102, s28, v84
	v_add_u32_e32 v118, s33, v84
	ds_read_b128 v[90:93], v102
	ds_read_b128 v[94:97], v102 offset:1024
	ds_read_b128 v[98:101], v102 offset:2048
	ds_read_b128 v[102:105], v102 offset:3072
	ds_read_b128 v[106:109], v118
	ds_read_b128 v[110:113], v118 offset:1024
	ds_read_b128 v[114:117], v118 offset:2048
	ds_read_b128 v[118:121], v118 offset:3072
	s_mov_b32 m0, s66
	v_lshl_add_u64 v[238:239], s[48:49], 0, v[8:9]
	ds_read_b128 v[158:161], v85 offset:32768
	ds_read_b128 v[170:173], v85 offset:33792
	ds_read_b128 v[186:189], v85 offset:34816
	ds_read_b128 v[190:193], v85 offset:35840
	ds_read_b128 v[196:199], v85 offset:36864
	ds_read_b128 v[200:203], v85 offset:37888
	ds_read_b128 v[208:211], v85 offset:38912
	ds_read_b128 v[228:231], v85 offset:39936
	global_load_lds_dwordx4 v[238:239], off
	v_lshl_add_u64 v[238:239], s[48:49], 0, v[78:79]
	s_mov_b32 m0, s67
	s_nop 0
	global_load_lds_dwordx4 v[238:239], off
	s_waitcnt vmcnt(8)
	s_waitcnt lgkmcnt(0)
	s_barrier
	v_mfma_f32_16x16x32_bf16 v[182:185], v[90:93], v[158:161], v[182:185]
	v_mfma_f32_16x16x32_bf16 v[178:181], v[98:101], v[158:161], v[178:181]
	v_mfma_f32_16x16x32_bf16 v[166:169], v[90:93], v[186:189], v[166:169]
	v_mfma_f32_16x16x32_bf16 v[162:165], v[98:101], v[186:189], v[162:165]
	v_mfma_f32_16x16x32_bf16 v[150:153], v[90:93], v[196:199], v[150:153]
	v_mfma_f32_16x16x32_bf16 v[146:149], v[98:101], v[196:199], v[146:149]
	v_mfma_f32_16x16x32_bf16 v[126:129], v[90:93], v[208:211], v[126:129]
	v_mfma_f32_16x16x32_bf16 v[122:125], v[98:101], v[208:211], v[122:125]
	v_mfma_f32_16x16x32_bf16 v[182:185], v[94:97], v[170:173], v[182:185]
	v_mfma_f32_16x16x32_bf16 v[178:181], v[102:105], v[170:173], v[178:181]
	v_mfma_f32_16x16x32_bf16 v[166:169], v[94:97], v[190:193], v[166:169]
	v_mfma_f32_16x16x32_bf16 v[162:165], v[102:105], v[190:193], v[162:165]
	v_mfma_f32_16x16x32_bf16 v[150:153], v[94:97], v[200:203], v[150:153]
	v_mfma_f32_16x16x32_bf16 v[146:149], v[102:105], v[200:203], v[146:149]
	v_mfma_f32_16x16x32_bf16 v[126:129], v[94:97], v[228:231], v[126:129]
	v_mfma_f32_16x16x32_bf16 v[122:125], v[102:105], v[228:231], v[122:125]
	v_mfma_f32_16x16x32_bf16 v[174:177], v[106:109], v[158:161], v[174:177]
	v_mfma_f32_16x16x32_bf16 v[130:133], v[114:117], v[158:161], v[130:133]
	v_mfma_f32_16x16x32_bf16 v[174:177], v[110:113], v[170:173], v[174:177]
	v_mfma_f32_16x16x32_bf16 v[170:173], v[118:121], v[170:173], v[130:133]
	v_mfma_f32_16x16x32_bf16 v[130:133], v[106:109], v[186:189], v[134:137]
	v_mfma_f32_16x16x32_bf16 v[158:161], v[110:113], v[190:193], v[130:133]
	v_mfma_f32_16x16x32_bf16 v[130:133], v[114:117], v[186:189], v[154:157]
	v_mfma_f32_16x16x32_bf16 v[154:157], v[118:121], v[190:193], v[130:133]
	v_mfma_f32_16x16x32_bf16 v[130:133], v[106:109], v[196:199], v[142:145]
	v_mfma_f32_16x16x32_bf16 v[142:145], v[110:113], v[200:203], v[130:133]
	v_mfma_f32_16x16x32_bf16 v[130:133], v[114:117], v[196:199], v[138:141]
	v_mfma_f32_16x16x32_bf16 v[86:89], v[106:109], v[208:211], v[86:89]
	v_mfma_f32_16x16x32_bf16 v[74:77], v[114:117], v[208:211], v[74:77]
	v_mfma_f32_16x16x32_bf16 v[138:141], v[118:121], v[200:203], v[130:133]
	v_mfma_f32_16x16x32_bf16 v[86:89], v[110:113], v[228:231], v[86:89]
	v_mfma_f32_16x16x32_bf16 v[74:77], v[118:121], v[228:231], v[74:77]
	s_barrier
; #define PG8_STAGE(bufoff, gbase, voff) do { _Pragma("unroll") for (int _i = 0; _i < 2; ++_i) \
;         __builtin_amdgcn_global_load_lds((const unsigned*)((const char*)(gbase) + (voff)[_i]), (LAS unsigned*)(lds + (bufoff) + ldsw + _i * 8192), 16, 0, 0); } while (0)
; #define PG8_LDA(dst, b, h) do { _Pragma("unroll") for (int m = 0; m < 4; ++m) _Pragma("unroll") for (int k = 0; k < 2; ++k) dst[m][k] = *(const LAS bf16x8*)(lds + PG8_SA(b, h) + aoff + m * 2048 + k * 1024); } while (0)
; #define PG8_MMA(ai, bj, At, Bt) do { __builtin_amdgcn_s_setprio(1); _Pragma("unroll") for (int m = 0; m < 4; ++m) _Pragma("unroll") for (int n = 0; n < 2; ++n) _Pragma("unroll") for (int k = 0; k < 2; ++k) \
;         acc[ai][bj][m][n] = __builtin_amdgcn_mfma_f32_16x16x32_bf16(Bt[n][k], At[m][k], acc[ai][bj][m][n], 0, 0, 0); __builtin_amdgcn_s_setprio(0); } while (0)
; #define PG8_WAIT_V(n) asm volatile("s_waitcnt vmcnt(" #n ")" ::: "memory")
; #define PG8_WAIT_L(n) asm volatile("s_waitcnt lgkmcnt(" #n ")" ::: "memory")
; #define PG8_BAR __builtin_amdgcn_s_barrier()
; #define PG8_SCHED __builtin_amdgcn_sched_barrier(0)
; template <class Epi, class Sched, bool GATHER = false>
; __device__ __forceinline__ void gemm_phase(LAS unsigned char* lds, const int lda, const int ldb, const int K, const Sched& S, const Epi& E, const int* gidx = nullptr) {
;     ...
;             PG8_LDA(At, 1, 1); PG8_STAGE(PG8_SB(1, 0), b3, voffB); PG8_STAGE(PG8_SB(1, 1), b3 + hstepB, voffB); PG8_STAGE(PG8_SA(1, 0), a3, o2[0]);
;             PG8_WAIT_V(8); PG8_WAIT_L(0); PG8_BAR; PG8_MMA(1, 0, At, B0); PG8_MMA(1, 1, At, B1); PG8_BAR; PG8_SCHED;
;         }
;         if (wr == 0) PG8_BAR;
	s_add_i32 s28, s28, s50
	v_lshl_add_u64 v[204:205], v[204:205], 0, s[64:65]
	s_mov_b32 m0, s28
	ds_read_b128 v[130:133], v85 offset:49152
	ds_read_b128 v[134:137], v85 offset:50176
	ds_read_b128 v[186:189], v85 offset:51200
	ds_read_b128 v[190:193], v85 offset:52224
	ds_read_b128 v[196:199], v85 offset:53248
	ds_read_b128 v[200:203], v85 offset:54272
	ds_read_b128 v[208:211], v85 offset:55296
	ds_read_b128 v[228:231], v85 offset:56320
	global_load_lds_dwordx4 v[204:205], off
	s_add_i32 m0, s28, 0x2000
	s_add_u32 s28, s34, 0x80080
	v_lshl_add_u64 v[204:205], v[232:233], 0, s[64:65]
	s_addc_u32 s29, s35, 0
	s_add_i32 s33, s33, s50
	global_load_lds_dwordx4 v[204:205], off
	v_lshl_add_u64 v[204:205], s[28:29], 0, v[194:195]
	s_mov_b32 m0, s33
	s_nop 0
	global_load_lds_dwordx4 v[204:205], off
	v_lshl_add_u64 v[204:205], s[28:29], 0, v[2:3]
	s_add_i32 m0, s33, 0x2000
	s_nop 0
	global_load_lds_dwordx4 v[204:205], off
	v_lshl_add_u64 v[204:205], v[234:235], 0, s[64:65]
	s_mov_b32 m0, s70
	s_nop 0
	global_load_lds_dwordx4 v[204:205], off
	v_lshl_add_u64 v[204:205], v[236:237], 0, s[64:65]
	s_mov_b32 m0, s71
	s_nop 0
	global_load_lds_dwordx4 v[204:205], off
	s_waitcnt vmcnt(8)
	s_waitcnt lgkmcnt(0)
	s_barrier
	v_mfma_f32_16x16x32_bf16 v[70:73], v[90:93], v[130:133], v[70:73]
	v_mfma_f32_16x16x32_bf16 v[66:69], v[98:101], v[130:133], v[66:69]
	v_mfma_f32_16x16x32_bf16 v[54:57], v[90:93], v[186:189], v[54:57]
	v_mfma_f32_16x16x32_bf16 v[46:49], v[98:101], v[186:189], v[46:49]
	v_mfma_f32_16x16x32_bf16 v[34:37], v[90:93], v[196:199], v[34:37]
	v_mfma_f32_16x16x32_bf16 v[26:29], v[98:101], v[196:199], v[26:29]
	v_mfma_f32_16x16x32_bf16 v[22:25], v[90:93], v[208:211], v[22:25]
	v_mfma_f32_16x16x32_bf16 v[18:21], v[98:101], v[208:211], v[18:21]
	v_mfma_f32_16x16x32_bf16 v[70:73], v[94:97], v[134:137], v[70:73]
	v_mfma_f32_16x16x32_bf16 v[66:69], v[102:105], v[134:137], v[66:69]
	v_mfma_f32_16x16x32_bf16 v[54:57], v[94:97], v[190:193], v[54:57]
	v_mfma_f32_16x16x32_bf16 v[46:49], v[102:105], v[190:193], v[46:49]
	v_mfma_f32_16x16x32_bf16 v[34:37], v[94:97], v[200:203], v[34:37]
	v_mfma_f32_16x16x32_bf16 v[26:29], v[102:105], v[200:203], v[26:29]
	v_mfma_f32_16x16x32_bf16 v[22:25], v[94:97], v[228:231], v[22:25]
	v_mfma_f32_16x16x32_bf16 v[18:21], v[102:105], v[228:231], v[18:21]
	v_mfma_f32_16x16x32_bf16 v[62:65], v[106:109], v[130:133], v[62:65]
	v_mfma_f32_16x16x32_bf16 v[58:61], v[114:117], v[130:133], v[58:61]
	v_mfma_f32_16x16x32_bf16 v[50:53], v[106:109], v[186:189], v[50:53]
	v_mfma_f32_16x16x32_bf16 v[42:45], v[114:117], v[186:189], v[42:45]
	v_mfma_f32_16x16x32_bf16 v[38:41], v[106:109], v[196:199], v[38:41]
	v_mfma_f32_16x16x32_bf16 v[30:33], v[114:117], v[196:199], v[30:33]
	v_mfma_f32_16x16x32_bf16 v[14:17], v[106:109], v[208:211], v[14:17]
	v_mfma_f32_16x16x32_bf16 v[10:13], v[114:117], v[208:211], v[10:13]
	v_mfma_f32_16x16x32_bf16 v[62:65], v[110:113], v[134:137], v[62:65]
	v_mfma_f32_16x16x32_bf16 v[58:61], v[118:121], v[134:137], v[58:61]
	v_mfma_f32_16x16x32_bf16 v[50:53], v[110:113], v[190:193], v[50:53]
	v_mfma_f32_16x16x32_bf16 v[42:45], v[118:121], v[190:193], v[42:45]
	v_mfma_f32_16x16x32_bf16 v[38:41], v[110:113], v[200:203], v[38:41]
	v_mfma_f32_16x16x32_bf16 v[30:33], v[118:121], v[200:203], v[30:33]
	v_mfma_f32_16x16x32_bf16 v[14:17], v[110:113], v[228:231], v[14:17]
	v_mfma_f32_16x16x32_bf16 v[10:13], v[118:121], v[228:231], v[10:13]
	s_barrier
	s_add_i32 s72, s72, 2
	s_add_u32 s12, s12, 0x100
	s_addc_u32 s13, s13, 0
	s_cmp_gt_u32 s72, 29
	s_cbranch_scc0 .LBB0_1186
	s_cmpk_lt_u32 s8, 0x100
	s_cbranch_scc0 .LBB0_1189
	s_barrier

; #define PG8_AOFF(of, u) do { _Pragma("unroll") for (int hh_ = 0; hh_ < 2; ++hh_) _Pragma("unroll") for (int i_ = 0; i_ < 2; ++i_) { \
;         if constexpr (GATHER) of[hh_][i_] = (unsigned)gidx[(u).pm * 256 + hh_ * 128 + RA[i_]] * (unsigned)(lda * 2) + CA2[i_]; \
;         else of[hh_][i_] = (unsigned)((hh_ * HALF + RA[i_]) * lda) * 2u + CA2[i_]; } } while (0)
; #define PG8_STAGE(bufoff, gbase, voff) do { _Pragma("unroll") for (int _i = 0; _i < 2; ++_i) \
;         __builtin_amdgcn_global_load_lds((const unsigned*)((const char*)(gbase) + (voff)[_i]), (LAS unsigned*)(lds + (bufoff) + ldsw + _i * 8192), 16, 0, 0); } while (0)
; #define PG8_LDA(dst, b, h) do { _Pragma("unroll") for (int m = 0; m < 4; ++m) _Pragma("unroll") for (int k = 0; k < 2; ++k) dst[m][k] = *(const LAS bf16x8*)(lds + PG8_SA(b, h) + aoff + m * 2048 + k * 1024); } while (0)
; #define PG8_WAIT_V(n) asm volatile("s_waitcnt vmcnt(" #n ")" ::: "memory")
; #define PG8_WAIT_L(n) asm volatile("s_waitcnt lgkmcnt(" #n ")" ::: "memory")
; template <class Epi, class Sched, bool GATHER = false>
; __device__ __forceinline__ void gemm_phase(LAS unsigned char* lds, const int lda, const int ldb, const int K, const Sched& S, const Epi& E, const int* gidx = nullptr) {
;     ...
;             const bool last = (t == nt - 2);
;             if constexpr (GATHER) { if (last && has_next) PG8_AOFF(ofn, nxt); }
;             const char* a1 = cA + (size_t)(t + 1) * kstep;
;             const char* a2 = last ? nA : cA + (size_t)(t + 2) * kstep; const char* b2 = last ? nB : cB + (size_t)(t + 2) * kstep;
;             const char* a3 = a2 + kstep; const char* b3 = b2 + kstep;
;             unsigned o2[2][2];
; #pragma unroll
;             for (int hh = 0; hh < 2; ++hh)
; #pragma unroll
;                 for (int i = 0; i < 2; ++i) { if constexpr (GATHER) o2[hh][i] = last ? ofn[hh][i] : ofc[hh][i]; else o2[hh][i] = ofc[hh][i]; }
;             PG8_LDB(B0, 0, 0); PG8_LDB(B1, 0, 1); PG8_SCHED; PG8_LDA(At, 0, 0); PG8_STAGE(PG8_SA(1, 1), a1, ofc[1]);
;             PG8_WAIT_V(8); PG8_WAIT_L(0); PG8_BAR; PG8_MMA(0, 0, At, B0); PG8_MMA(0, 1, At, B1); PG8_BAR; PG8_SCHED;
;             PG8_LDA(At, 0, 1); PG8_STAGE(PG8_SB(0, 0), b2, voffB); PG8_STAGE(PG8_SB(0, 1), b2 + hstepB, voffB); PG8_STAGE(PG8_SA(0, 0), a2, o2[0]);
;             PG8_WAIT_V(8); PG8_WAIT_L(0); PG8_BAR; PG8_MMA(1, 0, At, B0); PG8_MMA(1, 1, At, B1); PG8_BAR; PG8_SCHED;
.LBB0_1666:
	s_add_i32 s28, 0, 0x10000
	v_add_u32_e32 v135, s28, v159
	s_add_i32 s33, 0, 0x14000
	ds_read_b128 v[164:167], v135
	ds_read_b128 v[168:171], v135 offset:1024
	ds_read_b128 v[172:175], v135 offset:2048
	ds_read_b128 v[176:179], v135 offset:3072
	v_add_u32_e32 v135, s33, v159
	ds_read_b128 v[180:183], v135
	ds_read_b128 v[184:187], v135 offset:1024
	ds_read_b128 v[188:191], v135 offset:2048
	ds_read_b128 v[196:199], v135 offset:3072
	v_cndmask_b32_e64 v194, v138, v141, s[34:35]
	v_cndmask_b32_e64 v192, v136, v143, s[34:35]
	v_cndmask_b32_e64 v135, v140, v161, s[34:35]
	v_cndmask_b32_e64 v137, v142, v162, s[34:35]
	v_lshl_add_u64 v[222:223], v[154:155], 0, s[44:45]
	s_add_i32 m0, s10, 0xc000
	ds_read_b128 v[200:203], v160
	ds_read_b128 v[204:207], v160 offset:1024
	ds_read_b128 v[208:211], v160 offset:2048
	ds_read_b128 v[228:231], v160 offset:3072
	ds_read_b128 v[232:235], v160 offset:4096
	ds_read_b128 v[236:239], v160 offset:5120
	ds_read_b128 v[240:243], v160 offset:6144
	ds_read_b128 v[244:247], v160 offset:7168
	s_add_u32 s12, s26, s44
	s_addc_u32 s13, s27, s45
	s_add_u32 s28, s12, 0x24400100
	s_addc_u32 s29, s13, 0
	s_and_b64 s[12:13], s[34:35], exec
	s_cselect_b32 s49, s17, s29
	s_cselect_b32 s48, s16, s28
	s_add_u32 s28, s72, s44
	s_addc_u32 s29, s73, s45
	s_and_b64 s[12:13], s[34:35], exec
	s_cselect_b32 s13, s41, s29
	s_cselect_b32 s12, s40, s28
	s_add_i32 s28, 0, 0x10000
	global_load_lds_dwordx4 v[222:223], off
	v_lshl_add_u64 v[222:223], v[152:153], 0, s[44:45]
	s_add_i32 m0, s10, 0xe000
	s_nop 0
	global_load_lds_dwordx4 v[222:223], off
	s_waitcnt vmcnt(8)
	s_waitcnt lgkmcnt(0)
	s_barrier
	v_mfma_f32_16x16x32_bf16 v[126:129], v[164:167], v[200:203], v[126:129]
	v_mfma_f32_16x16x32_bf16 v[118:121], v[172:175], v[200:203], v[118:121]
	v_mfma_f32_16x16x32_bf16 v[110:113], v[164:167], v[208:211], v[110:113]
	v_mfma_f32_16x16x32_bf16 v[102:105], v[172:175], v[208:211], v[102:105]
	v_mfma_f32_16x16x32_bf16 v[94:97], v[164:167], v[232:235], v[94:97]
	v_mfma_f32_16x16x32_bf16 v[86:89], v[172:175], v[232:235], v[86:89]
	v_mfma_f32_16x16x32_bf16 v[78:81], v[164:167], v[240:243], v[78:81]
	v_mfma_f32_16x16x32_bf16 v[70:73], v[172:175], v[240:243], v[70:73]
	v_mfma_f32_16x16x32_bf16 v[126:129], v[168:171], v[204:207], v[126:129]
	v_mfma_f32_16x16x32_bf16 v[118:121], v[176:179], v[204:207], v[118:121]
	v_mfma_f32_16x16x32_bf16 v[110:113], v[168:171], v[228:231], v[110:113]
	v_mfma_f32_16x16x32_bf16 v[102:105], v[176:179], v[228:231], v[102:105]
	v_mfma_f32_16x16x32_bf16 v[94:97], v[168:171], v[236:239], v[94:97]
	v_mfma_f32_16x16x32_bf16 v[86:89], v[176:179], v[236:239], v[86:89]
	v_mfma_f32_16x16x32_bf16 v[78:81], v[168:171], v[244:247], v[78:81]
	v_mfma_f32_16x16x32_bf16 v[70:73], v[176:179], v[244:247], v[70:73]
	v_mfma_f32_16x16x32_bf16 v[122:125], v[180:183], v[200:203], v[122:125]
	v_mfma_f32_16x16x32_bf16 v[114:117], v[188:191], v[200:203], v[114:117]
	v_mfma_f32_16x16x32_bf16 v[106:109], v[180:183], v[208:211], v[106:109]
	v_mfma_f32_16x16x32_bf16 v[98:101], v[188:191], v[208:211], v[98:101]
	v_mfma_f32_16x16x32_bf16 v[90:93], v[180:183], v[232:235], v[90:93]
	v_mfma_f32_16x16x32_bf16 v[82:85], v[188:191], v[232:235], v[82:85]
	v_mfma_f32_16x16x32_bf16 v[74:77], v[180:183], v[240:243], v[74:77]
	v_mfma_f32_16x16x32_bf16 v[66:69], v[188:191], v[240:243], v[66:69]
	v_mfma_f32_16x16x32_bf16 v[122:125], v[184:187], v[204:207], v[122:125]
	v_mfma_f32_16x16x32_bf16 v[114:117], v[196:199], v[204:207], v[114:117]
	v_mfma_f32_16x16x32_bf16 v[106:109], v[184:187], v[228:231], v[106:109]
	v_mfma_f32_16x16x32_bf16 v[98:101], v[196:199], v[228:231], v[98:101]
	v_mfma_f32_16x16x32_bf16 v[90:93], v[184:187], v[236:239], v[90:93]
	v_mfma_f32_16x16x32_bf16 v[82:85], v[196:199], v[236:239], v[82:85]
	v_mfma_f32_16x16x32_bf16 v[74:77], v[184:187], v[244:247], v[74:77]
	v_mfma_f32_16x16x32_bf16 v[66:69], v[196:199], v[244:247], v[66:69]
	s_barrier
	s_add_i32 s28, s28, s9
	v_lshl_add_u64 v[222:223], s[12:13], 0, v[130:131]
	s_mov_b32 m0, s28
	ds_read_b128 v[200:203], v160 offset:16384
	ds_read_b128 v[204:207], v160 offset:17408
	ds_read_b128 v[208:211], v160 offset:18432
	ds_read_b128 v[228:231], v160 offset:19456
	ds_read_b128 v[232:235], v160 offset:20480
	ds_read_b128 v[236:239], v160 offset:21504
	ds_read_b128 v[240:243], v160 offset:22528
	ds_read_b128 v[244:247], v160 offset:23552
	global_load_lds_dwordx4 v[222:223], off
	s_add_i32 m0, s28, 0x2000
	s_add_u32 s28, s12, 0x80000
	v_lshl_add_u64 v[224:225], s[12:13], 0, v[132:133]
	s_addc_u32 s29, s13, 0
	s_add_i32 s33, s33, s9
	global_load_lds_dwordx4 v[224:225], off
	v_lshl_add_u64 v[214:215], s[28:29], 0, v[130:131]
	s_mov_b32 m0, s33
	v_mov_b32_e32 v193, v195
	global_load_lds_dwordx4 v[214:215], off
	v_lshl_add_u64 v[214:215], s[28:29], 0, v[132:133]
	s_add_i32 m0, s33, 0x2000
	s_nop 0
	global_load_lds_dwordx4 v[214:215], off
	s_mov_b32 m0, s10
	v_lshl_add_u64 v[214:215], s[48:49], 0, v[194:195]
	global_load_lds_dwordx4 v194, s[48:49]
	s_mov_b32 m0, s11
	s_nop 0
	global_load_lds_dwordx4 v192, s[48:49]
	s_waitcnt vmcnt(8)
	s_waitcnt lgkmcnt(0)
	v_lshl_add_u64 v[192:193], s[48:49], 0, v[192:193]
	s_barrier
; #define PG8_STAGE(bufoff, gbase, voff) do { _Pragma("unroll") for (int _i = 0; _i < 2; ++_i) \
;         __builtin_amdgcn_global_load_lds((const unsigned*)((const char*)(gbase) + (voff)[_i]), (LAS unsigned*)(lds + (bufoff) + ldsw + _i * 8192), 16, 0, 0); } while (0)
; #define PG8_LDA(dst, b, h) do { _Pragma("unroll") for (int m = 0; m < 4; ++m) _Pragma("unroll") for (int k = 0; k < 2; ++k) dst[m][k] = *(const LAS bf16x8*)(lds + PG8_SA(b, h) + aoff + m * 2048 + k * 1024); } while (0)
; #define PG8_LDB(dst, b, h) do { _Pragma("unroll") for (int n = 0; n < 2; ++n) _Pragma("unroll") for (int k = 0; k < 2; ++k) dst[n][k] = *(const LAS bf16x8*)(lds + PG8_SB(b, h) + boff + n * 2048 + k * 1024); } while (0)
; #define PG8_MMA(ai, bj, At, Bt) do { __builtin_amdgcn_s_setprio(1); _Pragma("unroll") for (int m = 0; m < 4; ++m) _Pragma("unroll") for (int n = 0; n < 2; ++n) _Pragma("unroll") for (int k = 0; k < 2; ++k) \
;         acc[ai][bj][m][n] = __builtin_amdgcn_mfma_f32_16x16x32_bf16(Bt[n][k], At[m][k], acc[ai][bj][m][n], 0, 0, 0); __builtin_amdgcn_s_setprio(0); } while (0)
; #define PG8_WAIT_V(n) asm volatile("s_waitcnt vmcnt(" #n ")" ::: "memory")
; #define PG8_WAIT_L(n) asm volatile("s_waitcnt lgkmcnt(" #n ")" ::: "memory")
; #define PG8_BAR __builtin_amdgcn_s_barrier()
; #define PG8_SCHED __builtin_amdgcn_sched_barrier(0)
; template <class Epi, class Sched, bool GATHER = false>
; __device__ __forceinline__ void gemm_phase(LAS unsigned char* lds, const int lda, const int ldb, const int K, const Sched& S, const Epi& E, const int* gidx = nullptr) {
;     ...
;             PG8_WAIT_V(8); PG8_WAIT_L(0); PG8_BAR; PG8_MMA(1, 0, At, B0); PG8_MMA(1, 1, At, B1); PG8_BAR; PG8_SCHED;
;             PG8_LDB(B0, 1, 0); PG8_LDB(B1, 1, 1); PG8_SCHED; PG8_LDA(At, 1, 0); PG8_STAGE(PG8_SA(0, 1), a2, o2[1]);
;             PG8_WAIT_V(8); PG8_WAIT_L(0); PG8_BAR; PG8_MMA(0, 0, At, B0); PG8_MMA(0, 1, At, B1); PG8_BAR; PG8_SCHED;
	v_mfma_f32_16x16x32_bf16 v[62:65], v[164:167], v[200:203], v[62:65]
	v_mfma_f32_16x16x32_bf16 v[54:57], v[172:175], v[200:203], v[54:57]
	v_mfma_f32_16x16x32_bf16 v[46:49], v[164:167], v[208:211], v[46:49]
	v_mfma_f32_16x16x32_bf16 v[38:41], v[172:175], v[208:211], v[38:41]
	v_mfma_f32_16x16x32_bf16 v[22:25], v[164:167], v[232:235], v[22:25]
	v_mfma_f32_16x16x32_bf16 v[18:21], v[172:175], v[232:235], v[18:21]
	v_mfma_f32_16x16x32_bf16 v[6:9], v[164:167], v[240:243], v[6:9]
	v_mfma_f32_16x16x32_bf16 v[2:5], v[172:175], v[240:243], v[2:5]
	v_mfma_f32_16x16x32_bf16 v[62:65], v[168:171], v[204:207], v[62:65]
	v_mfma_f32_16x16x32_bf16 v[54:57], v[176:179], v[204:207], v[54:57]
	v_mfma_f32_16x16x32_bf16 v[46:49], v[168:171], v[228:231], v[46:49]
	v_mfma_f32_16x16x32_bf16 v[38:41], v[176:179], v[228:231], v[38:41]
	v_mfma_f32_16x16x32_bf16 v[22:25], v[168:171], v[236:239], v[22:25]
	v_mfma_f32_16x16x32_bf16 v[18:21], v[176:179], v[236:239], v[18:21]
	v_mfma_f32_16x16x32_bf16 v[6:9], v[168:171], v[244:247], v[6:9]
	v_mfma_f32_16x16x32_bf16 v[2:5], v[176:179], v[244:247], v[2:5]
	v_mfma_f32_16x16x32_bf16 v[58:61], v[180:183], v[200:203], v[58:61]
	v_mfma_f32_16x16x32_bf16 v[50:53], v[188:191], v[200:203], v[50:53]
	v_mfma_f32_16x16x32_bf16 v[42:45], v[180:183], v[208:211], v[42:45]
	v_mfma_f32_16x16x32_bf16 v[34:37], v[188:191], v[208:211], v[34:37]
	v_mfma_f32_16x16x32_bf16 v[30:33], v[180:183], v[232:235], v[30:33]
	v_mfma_f32_16x16x32_bf16 v[26:29], v[188:191], v[232:235], v[26:29]
	v_mfma_f32_16x16x32_bf16 v[14:17], v[180:183], v[240:243], v[14:17]
	v_mfma_f32_16x16x32_bf16 v[10:13], v[188:191], v[240:243], v[10:13]
	v_mfma_f32_16x16x32_bf16 v[58:61], v[184:187], v[204:207], v[58:61]
	v_mfma_f32_16x16x32_bf16 v[50:53], v[196:199], v[204:207], v[50:53]
	v_mfma_f32_16x16x32_bf16 v[42:45], v[184:187], v[228:231], v[42:45]
	v_mfma_f32_16x16x32_bf16 v[34:37], v[196:199], v[228:231], v[34:37]
	v_mfma_f32_16x16x32_bf16 v[30:33], v[184:187], v[236:239], v[30:33]
	v_mfma_f32_16x16x32_bf16 v[26:29], v[196:199], v[236:239], v[26:29]
	v_mfma_f32_16x16x32_bf16 v[14:17], v[184:187], v[244:247], v[14:17]
	v_mfma_f32_16x16x32_bf16 v[10:13], v[196:199], v[244:247], v[10:13]
	s_barrier
	s_add_i32 s28, 0, 0x18000
	v_add_u32_e32 v163, s28, v159
	s_add_i32 s29, 0, 0x1c000
	ds_read_b128 v[164:167], v163
	ds_read_b128 v[168:171], v163 offset:1024
	ds_read_b128 v[172:175], v163 offset:2048
	ds_read_b128 v[176:179], v163 offset:3072
	v_add_u32_e32 v163, s29, v159
	ds_read_b128 v[180:183], v163
	ds_read_b128 v[184:187], v163 offset:1024
	ds_read_b128 v[188:191], v163 offset:2048
	ds_read_b128 v[196:199], v163 offset:3072
	s_mov_b32 m0, s22
	ds_read_b128 v[200:203], v160 offset:32768
	ds_read_b128 v[204:207], v160 offset:33792
	ds_read_b128 v[208:211], v160 offset:34816
	ds_read_b128 v[228:231], v160 offset:35840
	ds_read_b128 v[232:235], v160 offset:36864
	ds_read_b128 v[236:239], v160 offset:37888
	ds_read_b128 v[240:243], v160 offset:38912
	ds_read_b128 v[244:247], v160 offset:39936
	global_load_lds_dwordx4 v135, s[48:49]
	s_mov_b32 m0, s23
	s_nop 0
	global_load_lds_dwordx4 v137, s[48:49]
	s_waitcnt vmcnt(8)
	s_waitcnt lgkmcnt(0)
	s_barrier
	v_mfma_f32_16x16x32_bf16 v[126:129], v[164:167], v[200:203], v[126:129]
	v_mfma_f32_16x16x32_bf16 v[118:121], v[172:175], v[200:203], v[118:121]
	v_mfma_f32_16x16x32_bf16 v[110:113], v[164:167], v[208:211], v[110:113]
	v_mfma_f32_16x16x32_bf16 v[102:105], v[172:175], v[208:211], v[102:105]
	v_mfma_f32_16x16x32_bf16 v[94:97], v[164:167], v[232:235], v[94:97]
	v_mfma_f32_16x16x32_bf16 v[86:89], v[172:175], v[232:235], v[86:89]
	v_mfma_f32_16x16x32_bf16 v[78:81], v[164:167], v[240:243], v[78:81]
	v_mfma_f32_16x16x32_bf16 v[70:73], v[172:175], v[240:243], v[70:73]
	v_mfma_f32_16x16x32_bf16 v[126:129], v[168:171], v[204:207], v[126:129]
	v_mfma_f32_16x16x32_bf16 v[118:121], v[176:179], v[204:207], v[118:121]
	v_mfma_f32_16x16x32_bf16 v[110:113], v[168:171], v[228:231], v[110:113]
	v_mfma_f32_16x16x32_bf16 v[102:105], v[176:179], v[228:231], v[102:105]
	v_mfma_f32_16x16x32_bf16 v[94:97], v[168:171], v[236:239], v[94:97]
	v_mfma_f32_16x16x32_bf16 v[86:89], v[176:179], v[236:239], v[86:89]
	v_mfma_f32_16x16x32_bf16 v[78:81], v[168:171], v[244:247], v[78:81]
	v_mfma_f32_16x16x32_bf16 v[70:73], v[176:179], v[244:247], v[70:73]
	v_mfma_f32_16x16x32_bf16 v[122:125], v[180:183], v[200:203], v[122:125]
	v_mfma_f32_16x16x32_bf16 v[114:117], v[188:191], v[200:203], v[114:117]
	v_mfma_f32_16x16x32_bf16 v[106:109], v[180:183], v[208:211], v[106:109]
	v_mfma_f32_16x16x32_bf16 v[98:101], v[188:191], v[208:211], v[98:101]
	v_mfma_f32_16x16x32_bf16 v[90:93], v[180:183], v[232:235], v[90:93]
	v_mfma_f32_16x16x32_bf16 v[82:85], v[188:191], v[232:235], v[82:85]
	v_mfma_f32_16x16x32_bf16 v[74:77], v[180:183], v[240:243], v[74:77]
	v_mfma_f32_16x16x32_bf16 v[66:69], v[188:191], v[240:243], v[66:69]
	v_mfma_f32_16x16x32_bf16 v[122:125], v[184:187], v[204:207], v[122:125]
	v_mfma_f32_16x16x32_bf16 v[114:117], v[196:199], v[204:207], v[114:117]
	v_mfma_f32_16x16x32_bf16 v[106:109], v[184:187], v[228:231], v[106:109]
	v_mfma_f32_16x16x32_bf16 v[98:101], v[196:199], v[228:231], v[98:101]
	v_mfma_f32_16x16x32_bf16 v[90:93], v[184:187], v[236:239], v[90:93]
	v_mfma_f32_16x16x32_bf16 v[82:85], v[196:199], v[236:239], v[82:85]
	v_mfma_f32_16x16x32_bf16 v[74:77], v[184:187], v[244:247], v[74:77]
	v_mfma_f32_16x16x32_bf16 v[66:69], v[196:199], v[244:247], v[66:69]
	s_barrier
; #define PG8_STAGE(bufoff, gbase, voff) do { _Pragma("unroll") for (int _i = 0; _i < 2; ++_i) \
;         __builtin_amdgcn_global_load_lds((const unsigned*)((const char*)(gbase) + (voff)[_i]), (LAS unsigned*)(lds + (bufoff) + ldsw + _i * 8192), 16, 0, 0); } while (0)
; #define PG8_LDA(dst, b, h) do { _Pragma("unroll") for (int m = 0; m < 4; ++m) _Pragma("unroll") for (int k = 0; k < 2; ++k) dst[m][k] = *(const LAS bf16x8*)(lds + PG8_SA(b, h) + aoff + m * 2048 + k * 1024); } while (0)
; #define PG8_MMA(ai, bj, At, Bt) do { __builtin_amdgcn_s_setprio(1); _Pragma("unroll") for (int m = 0; m < 4; ++m) _Pragma("unroll") for (int n = 0; n < 2; ++n) _Pragma("unroll") for (int k = 0; k < 2; ++k) \
;         acc[ai][bj][m][n] = __builtin_amdgcn_mfma_f32_16x16x32_bf16(Bt[n][k], At[m][k], acc[ai][bj][m][n], 0, 0, 0); __builtin_amdgcn_s_setprio(0); } while (0)
; #define PG8_WAIT_V(n) asm volatile("s_waitcnt vmcnt(" #n ")" ::: "memory")
; #define PG8_WAIT_L(n) asm volatile("s_waitcnt lgkmcnt(" #n ")" ::: "memory")
; #define PG8_BAR __builtin_amdgcn_s_barrier()
; #define PG8_SCHED __builtin_amdgcn_sched_barrier(0)
; template <class Epi, class Sched, bool GATHER = false>
; __device__ __forceinline__ void gemm_phase(LAS unsigned char* lds, const int lda, const int ldb, const int K, const Sched& S, const Epi& E, const int* gidx = nullptr) {
;     ...
;             PG8_LDA(At, 1, 1); PG8_STAGE(PG8_SB(1, 0), b3, voffB); PG8_STAGE(PG8_SB(1, 1), b3 + hstepB, voffB); PG8_STAGE(PG8_SA(1, 0), a3, o2[0]);
;             PG8_WAIT_V(8); PG8_WAIT_L(0); PG8_BAR; PG8_MMA(1, 0, At, B0); PG8_MMA(1, 1, At, B1); PG8_BAR; PG8_SCHED;
;         }
	s_add_i32 s28, s28, s9
	v_lshl_add_u64 v[222:223], v[222:223], 0, s[64:65]
	s_mov_b32 m0, s28
	ds_read_b128 v[200:203], v160 offset:49152
	ds_read_b128 v[204:207], v160 offset:50176
	ds_read_b128 v[208:211], v160 offset:51200
	ds_read_b128 v[228:231], v160 offset:52224
	ds_read_b128 v[232:235], v160 offset:53248
	ds_read_b128 v[236:239], v160 offset:54272
	ds_read_b128 v[240:243], v160 offset:55296
	ds_read_b128 v[244:247], v160 offset:56320
	global_load_lds_dwordx4 v[222:223], off
	s_add_i32 m0, s28, 0x2000
	s_add_u32 s12, s12, 0x80080
	v_lshl_add_u64 v[222:223], v[224:225], 0, s[64:65]
	s_addc_u32 s13, s13, 0
	s_add_i32 s28, s29, s9
	global_load_lds_dwordx4 v[222:223], off
	v_lshl_add_u64 v[222:223], s[12:13], 0, v[130:131]
	s_mov_b32 m0, s28
	v_lshl_add_u64 v[214:215], v[214:215], 0, s[64:65]
	global_load_lds_dwordx4 v[222:223], off
	v_lshl_add_u64 v[222:223], s[12:13], 0, v[132:133]
	s_add_i32 m0, s28, 0x2000
	v_lshl_add_u64 v[192:193], v[192:193], 0, s[64:65]
	global_load_lds_dwordx4 v[222:223], off
	s_mov_b32 m0, s50
	s_nop 0
	global_load_lds_dwordx4 v[214:215], off
	s_mov_b32 m0, s51
	s_nop 0
	global_load_lds_dwordx4 v[192:193], off
	s_waitcnt vmcnt(8)
	s_waitcnt lgkmcnt(0)
	s_barrier
	v_mfma_f32_16x16x32_bf16 v[62:65], v[164:167], v[200:203], v[62:65]
	v_mfma_f32_16x16x32_bf16 v[54:57], v[172:175], v[200:203], v[54:57]
	v_mfma_f32_16x16x32_bf16 v[46:49], v[164:167], v[208:211], v[46:49]
	v_mfma_f32_16x16x32_bf16 v[38:41], v[172:175], v[208:211], v[38:41]
	v_mfma_f32_16x16x32_bf16 v[22:25], v[164:167], v[232:235], v[22:25]
	v_mfma_f32_16x16x32_bf16 v[18:21], v[172:175], v[232:235], v[18:21]
	v_mfma_f32_16x16x32_bf16 v[6:9], v[164:167], v[240:243], v[6:9]
	v_mfma_f32_16x16x32_bf16 v[2:5], v[172:175], v[240:243], v[2:5]
	v_mfma_f32_16x16x32_bf16 v[62:65], v[168:171], v[204:207], v[62:65]
	v_mfma_f32_16x16x32_bf16 v[54:57], v[176:179], v[204:207], v[54:57]
	v_mfma_f32_16x16x32_bf16 v[46:49], v[168:171], v[228:231], v[46:49]
	v_mfma_f32_16x16x32_bf16 v[38:41], v[176:179], v[228:231], v[38:41]
	v_mfma_f32_16x16x32_bf16 v[22:25], v[168:171], v[236:239], v[22:25]
	v_mfma_f32_16x16x32_bf16 v[18:21], v[176:179], v[236:239], v[18:21]
	v_mfma_f32_16x16x32_bf16 v[6:9], v[168:171], v[244:247], v[6:9]
	v_mfma_f32_16x16x32_bf16 v[2:5], v[176:179], v[244:247], v[2:5]
	v_mfma_f32_16x16x32_bf16 v[58:61], v[180:183], v[200:203], v[58:61]
	v_mfma_f32_16x16x32_bf16 v[50:53], v[188:191], v[200:203], v[50:53]
	v_mfma_f32_16x16x32_bf16 v[42:45], v[180:183], v[208:211], v[42:45]
	v_mfma_f32_16x16x32_bf16 v[34:37], v[188:191], v[208:211], v[34:37]
	v_mfma_f32_16x16x32_bf16 v[30:33], v[180:183], v[232:235], v[30:33]
	v_mfma_f32_16x16x32_bf16 v[26:29], v[188:191], v[232:235], v[26:29]
	v_mfma_f32_16x16x32_bf16 v[14:17], v[180:183], v[240:243], v[14:17]
	v_mfma_f32_16x16x32_bf16 v[10:13], v[188:191], v[240:243], v[10:13]
	v_mfma_f32_16x16x32_bf16 v[58:61], v[184:187], v[204:207], v[58:61]
	v_mfma_f32_16x16x32_bf16 v[50:53], v[196:199], v[204:207], v[50:53]
	v_mfma_f32_16x16x32_bf16 v[42:45], v[184:187], v[228:231], v[42:45]
	v_mfma_f32_16x16x32_bf16 v[34:37], v[196:199], v[228:231], v[34:37]
	v_mfma_f32_16x16x32_bf16 v[30:33], v[184:187], v[236:239], v[30:33]
	v_mfma_f32_16x16x32_bf16 v[26:29], v[196:199], v[236:239], v[26:29]
	v_mfma_f32_16x16x32_bf16 v[14:17], v[184:187], v[244:247], v[14:17]
	v_mfma_f32_16x16x32_bf16 v[10:13], v[196:199], v[244:247], v[10:13]
	s_barrier
	s_add_i32 s74, s74, 2
	s_add_u32 s44, s44, 0x100
	s_addc_u32 s45, s45, 0
	s_cmp_gt_u32 s74, 29
	s_cbranch_scc1 .LBB0_1669

; #define PG8_AOFF(of, u) do { _Pragma("unroll") for (int hh_ = 0; hh_ < 2; ++hh_) _Pragma("unroll") for (int i_ = 0; i_ < 2; ++i_) { \
;         if constexpr (GATHER) of[hh_][i_] = (unsigned)gidx[(u).pm * 256 + hh_ * 128 + RA[i_]] * (unsigned)(lda * 2) + CA2[i_]; \
;         else of[hh_][i_] = (unsigned)((hh_ * HALF + RA[i_]) * lda) * 2u + CA2[i_]; } } while (0)
; #define PG8_STAGE(bufoff, gbase, voff) do { _Pragma("unroll") for (int _i = 0; _i < 2; ++_i) \
;         __builtin_amdgcn_global_load_lds((const unsigned*)((const char*)(gbase) + (voff)[_i]), (LAS unsigned*)(lds + (bufoff) + ldsw + _i * 8192), 16, 0, 0); } while (0)
; #define PG8_LDA(dst, b, h) do { _Pragma("unroll") for (int m = 0; m < 4; ++m) _Pragma("unroll") for (int k = 0; k < 2; ++k) dst[m][k] = *(const LAS bf16x8*)(lds + PG8_SA(b, h) + aoff + m * 2048 + k * 1024); } while (0)
; #define PG8_WAIT_V(n) asm volatile("s_waitcnt vmcnt(" #n ")" ::: "memory")
; #define PG8_WAIT_L(n) asm volatile("s_waitcnt lgkmcnt(" #n ")" ::: "memory")
; template <class Epi, class Sched, bool GATHER = false>
; __device__ __forceinline__ void gemm_phase(LAS unsigned char* lds, const int lda, const int ldb, const int K, const Sched& S, const Epi& E, const int* gidx = nullptr) {
;     ...
;             const bool last = (t == nt - 2);
;             if constexpr (GATHER) { if (last && has_next) PG8_AOFF(ofn, nxt); }
;             const char* a1 = cA + (size_t)(t + 1) * kstep;
;             const char* a2 = last ? nA : cA + (size_t)(t + 2) * kstep; const char* b2 = last ? nB : cB + (size_t)(t + 2) * kstep;
;             const char* a3 = a2 + kstep; const char* b3 = b2 + kstep;
;             unsigned o2[2][2];
; #pragma unroll
;             for (int hh = 0; hh < 2; ++hh)
; #pragma unroll
;                 for (int i = 0; i < 2; ++i) { if constexpr (GATHER) o2[hh][i] = last ? ofn[hh][i] : ofc[hh][i]; else o2[hh][i] = ofc[hh][i]; }
;             PG8_LDB(B0, 0, 0); PG8_LDB(B1, 0, 1); PG8_SCHED; PG8_LDA(At, 0, 0); PG8_STAGE(PG8_SA(1, 1), a1, ofc[1]);
;             PG8_WAIT_V(8); PG8_WAIT_L(0); PG8_BAR; PG8_MMA(0, 0, At, B0); PG8_MMA(0, 1, At, B1); PG8_BAR; PG8_SCHED;
;             PG8_LDA(At, 0, 1); PG8_STAGE(PG8_SB(0, 0), b2, voffB); PG8_STAGE(PG8_SB(0, 1), b2 + hstepB, voffB); PG8_STAGE(PG8_SA(0, 0), a2, o2[0]);
;             PG8_WAIT_V(8); PG8_WAIT_L(0); PG8_BAR; PG8_MMA(1, 0, At, B0); PG8_MMA(1, 1, At, B1); PG8_BAR; PG8_SCHED;
.LBB0_1733:
	s_add_i32 s28, 0, 0x10000
	v_add_u32_e32 v146, s28, v147
	s_add_i32 s33, 0, 0x14000
	ds_read_b128 v[152:155], v146
	ds_read_b128 v[156:159], v146 offset:1024
	ds_read_b128 v[160:163], v146 offset:2048
	ds_read_b128 v[164:167], v146 offset:3072
	v_add_u32_e32 v146, s33, v147
	ds_read_b128 v[168:171], v146
	ds_read_b128 v[172:175], v146 offset:1024
	ds_read_b128 v[176:179], v146 offset:2048
	ds_read_b128 v[180:183], v146 offset:3072
	v_lshl_add_u64 v[148:149], s[44:45], 0, v[144:145]
	s_add_i32 m0, s10, 0xc000
	ds_read_b128 v[184:187], v151
	ds_read_b128 v[188:191], v151 offset:1024
	ds_read_b128 v[196:199], v151 offset:2048
	ds_read_b128 v[200:203], v151 offset:3072
	ds_read_b128 v[204:207], v151 offset:4096
	ds_read_b128 v[208:211], v151 offset:5120
	ds_read_b128 v[228:231], v151 offset:6144
	ds_read_b128 v[232:235], v151 offset:7168
	s_add_u32 s12, s44, 0x80
	s_addc_u32 s13, s45, 0
	s_cmp_eq_u32 s72, 12
	s_cselect_b32 s49, s39, s13
	s_cselect_b32 s48, s38, s12
	s_cselect_b32 s13, s41, s71
	s_cselect_b32 s12, s40, s70
	global_load_lds_dwordx4 v[148:149], off
	v_lshl_add_u64 v[148:149], s[44:45], 0, v[142:143]
	s_add_i32 m0, s10, 0xe000
	s_nop 0
	global_load_lds_dwordx4 v[148:149], off
	s_waitcnt vmcnt(8)
	s_waitcnt lgkmcnt(0)
	s_barrier
	v_mfma_f32_16x16x32_bf16 v[126:129], v[152:155], v[184:187], v[126:129]
	v_mfma_f32_16x16x32_bf16 v[122:125], v[160:163], v[184:187], v[122:125]
	v_mfma_f32_16x16x32_bf16 v[110:113], v[152:155], v[196:199], v[110:113]
	v_mfma_f32_16x16x32_bf16 v[106:109], v[160:163], v[196:199], v[106:109]
	v_mfma_f32_16x16x32_bf16 v[94:97], v[152:155], v[204:207], v[94:97]
	v_mfma_f32_16x16x32_bf16 v[90:93], v[160:163], v[204:207], v[90:93]
	v_mfma_f32_16x16x32_bf16 v[82:85], v[152:155], v[228:231], v[82:85]
	v_mfma_f32_16x16x32_bf16 v[74:77], v[160:163], v[228:231], v[74:77]
	v_mfma_f32_16x16x32_bf16 v[126:129], v[156:159], v[188:191], v[126:129]
	v_mfma_f32_16x16x32_bf16 v[122:125], v[164:167], v[188:191], v[122:125]
	v_mfma_f32_16x16x32_bf16 v[110:113], v[156:159], v[200:203], v[110:113]
	v_mfma_f32_16x16x32_bf16 v[106:109], v[164:167], v[200:203], v[106:109]
	v_mfma_f32_16x16x32_bf16 v[94:97], v[156:159], v[208:211], v[94:97]
	v_mfma_f32_16x16x32_bf16 v[90:93], v[164:167], v[208:211], v[90:93]
	v_mfma_f32_16x16x32_bf16 v[82:85], v[156:159], v[232:235], v[82:85]
	v_mfma_f32_16x16x32_bf16 v[74:77], v[164:167], v[232:235], v[74:77]
	v_mfma_f32_16x16x32_bf16 v[118:121], v[168:171], v[184:187], v[118:121]
	v_mfma_f32_16x16x32_bf16 v[114:117], v[176:179], v[184:187], v[114:117]
	v_mfma_f32_16x16x32_bf16 v[102:105], v[168:171], v[196:199], v[102:105]
	v_mfma_f32_16x16x32_bf16 v[98:101], v[176:179], v[196:199], v[98:101]
	v_mfma_f32_16x16x32_bf16 v[86:89], v[168:171], v[204:207], v[86:89]
	v_mfma_f32_16x16x32_bf16 v[78:81], v[176:179], v[204:207], v[78:81]
	v_mfma_f32_16x16x32_bf16 v[62:65], v[168:171], v[228:231], v[62:65]
	v_mfma_f32_16x16x32_bf16 v[58:61], v[176:179], v[228:231], v[58:61]
	v_mfma_f32_16x16x32_bf16 v[118:121], v[172:175], v[188:191], v[118:121]
	v_mfma_f32_16x16x32_bf16 v[114:117], v[180:183], v[188:191], v[114:117]
	v_mfma_f32_16x16x32_bf16 v[102:105], v[172:175], v[200:203], v[102:105]
	v_mfma_f32_16x16x32_bf16 v[98:101], v[180:183], v[200:203], v[98:101]
	v_mfma_f32_16x16x32_bf16 v[86:89], v[172:175], v[208:211], v[86:89]
	v_mfma_f32_16x16x32_bf16 v[78:81], v[180:183], v[208:211], v[78:81]
	v_mfma_f32_16x16x32_bf16 v[62:65], v[172:175], v[232:235], v[62:65]
	v_mfma_f32_16x16x32_bf16 v[58:61], v[180:183], v[232:235], v[58:61]
	s_barrier
	s_add_i32 s28, s28, s9
	v_lshl_add_u64 v[148:149], s[12:13], 0, v[132:133]
	s_mov_b32 m0, s28
	ds_read_b128 v[184:187], v151 offset:16384
	ds_read_b128 v[188:191], v151 offset:17408
	ds_read_b128 v[196:199], v151 offset:18432
	ds_read_b128 v[200:203], v151 offset:19456
	ds_read_b128 v[204:207], v151 offset:20480
	ds_read_b128 v[208:211], v151 offset:21504
	ds_read_b128 v[228:231], v151 offset:22528
	ds_read_b128 v[232:235], v151 offset:23552
	global_load_lds_dwordx4 v[148:149], off
	s_add_i32 m0, s28, 0x2000
	s_add_u32 s28, s12, 0x40000
	v_lshl_add_u64 v[192:193], s[12:13], 0, v[130:131]
	s_addc_u32 s29, s13, 0
	s_add_i32 s33, s33, s9
	global_load_lds_dwordx4 v[192:193], off
	v_lshl_add_u64 v[214:215], s[28:29], 0, v[132:133]
	s_mov_b32 m0, s33
	v_lshl_add_u64 v[222:223], s[48:49], 0, v[136:137]
	global_load_lds_dwordx4 v[214:215], off
	v_lshl_add_u64 v[214:215], s[28:29], 0, v[130:131]
	s_add_i32 m0, s33, 0x2000
	s_nop 0
	global_load_lds_dwordx4 v[214:215], off
	v_lshl_add_u64 v[214:215], s[48:49], 0, v[134:135]
	s_mov_b32 m0, s10
	s_nop 0
	global_load_lds_dwordx4 v[214:215], off
	s_mov_b32 m0, s11
	s_nop 0
	global_load_lds_dwordx4 v[222:223], off
	s_waitcnt vmcnt(8)
	s_waitcnt lgkmcnt(0)
	s_barrier
; #define PG8_STAGE(bufoff, gbase, voff) do { _Pragma("unroll") for (int _i = 0; _i < 2; ++_i) \
;         __builtin_amdgcn_global_load_lds((const unsigned*)((const char*)(gbase) + (voff)[_i]), (LAS unsigned*)(lds + (bufoff) + ldsw + _i * 8192), 16, 0, 0); } while (0)
; #define PG8_LDA(dst, b, h) do { _Pragma("unroll") for (int m = 0; m < 4; ++m) _Pragma("unroll") for (int k = 0; k < 2; ++k) dst[m][k] = *(const LAS bf16x8*)(lds + PG8_SA(b, h) + aoff + m * 2048 + k * 1024); } while (0)
; #define PG8_LDB(dst, b, h) do { _Pragma("unroll") for (int n = 0; n < 2; ++n) _Pragma("unroll") for (int k = 0; k < 2; ++k) dst[n][k] = *(const LAS bf16x8*)(lds + PG8_SB(b, h) + boff + n * 2048 + k * 1024); } while (0)
; #define PG8_MMA(ai, bj, At, Bt) do { __builtin_amdgcn_s_setprio(1); _Pragma("unroll") for (int m = 0; m < 4; ++m) _Pragma("unroll") for (int n = 0; n < 2; ++n) _Pragma("unroll") for (int k = 0; k < 2; ++k) \
;         acc[ai][bj][m][n] = __builtin_amdgcn_mfma_f32_16x16x32_bf16(Bt[n][k], At[m][k], acc[ai][bj][m][n], 0, 0, 0); __builtin_amdgcn_s_setprio(0); } while (0)
; #define PG8_WAIT_V(n) asm volatile("s_waitcnt vmcnt(" #n ")" ::: "memory")
; #define PG8_WAIT_L(n) asm volatile("s_waitcnt lgkmcnt(" #n ")" ::: "memory")
; #define PG8_BAR __builtin_amdgcn_s_barrier()
; #define PG8_SCHED __builtin_amdgcn_sched_barrier(0)
; template <class Epi, class Sched, bool GATHER = false>
; __device__ __forceinline__ void gemm_phase(LAS unsigned char* lds, const int lda, const int ldb, const int K, const Sched& S, const Epi& E, const int* gidx = nullptr) {
;     ...
;             PG8_WAIT_V(8); PG8_WAIT_L(0); PG8_BAR; PG8_MMA(1, 0, At, B0); PG8_MMA(1, 1, At, B1); PG8_BAR; PG8_SCHED;
;             PG8_LDB(B0, 1, 0); PG8_LDB(B1, 1, 1); PG8_SCHED; PG8_LDA(At, 1, 0); PG8_STAGE(PG8_SA(0, 1), a2, o2[1]);
;             PG8_WAIT_V(8); PG8_WAIT_L(0); PG8_BAR; PG8_MMA(0, 0, At, B0); PG8_MMA(0, 1, At, B1); PG8_BAR; PG8_SCHED;
	v_mfma_f32_16x16x32_bf16 v[54:57], v[152:155], v[184:187], v[54:57]
	v_mfma_f32_16x16x32_bf16 v[50:53], v[160:163], v[184:187], v[50:53]
	v_mfma_f32_16x16x32_bf16 v[30:33], v[152:155], v[196:199], v[30:33]
	v_mfma_f32_16x16x32_bf16 v[26:29], v[160:163], v[196:199], v[26:29]
	v_mfma_f32_16x16x32_bf16 v[14:17], v[152:155], v[204:207], v[14:17]
	v_mfma_f32_16x16x32_bf16 v[10:13], v[160:163], v[204:207], v[10:13]
	v_mfma_f32_16x16x32_bf16 v[6:9], v[152:155], v[228:231], v[6:9]
	v_mfma_f32_16x16x32_bf16 v[2:5], v[160:163], v[228:231], v[2:5]
	v_mfma_f32_16x16x32_bf16 v[54:57], v[156:159], v[188:191], v[54:57]
	v_mfma_f32_16x16x32_bf16 v[50:53], v[164:167], v[188:191], v[50:53]
	v_mfma_f32_16x16x32_bf16 v[30:33], v[156:159], v[200:203], v[30:33]
	v_mfma_f32_16x16x32_bf16 v[26:29], v[164:167], v[200:203], v[26:29]
	v_mfma_f32_16x16x32_bf16 v[14:17], v[156:159], v[208:211], v[14:17]
	v_mfma_f32_16x16x32_bf16 v[10:13], v[164:167], v[208:211], v[10:13]
	v_mfma_f32_16x16x32_bf16 v[6:9], v[156:159], v[232:235], v[6:9]
	v_mfma_f32_16x16x32_bf16 v[2:5], v[164:167], v[232:235], v[2:5]
	v_mfma_f32_16x16x32_bf16 v[66:69], v[168:171], v[184:187], v[66:69]
	v_mfma_f32_16x16x32_bf16 v[70:73], v[176:179], v[184:187], v[70:73]
	v_mfma_f32_16x16x32_bf16 v[42:45], v[168:171], v[196:199], v[42:45]
	v_mfma_f32_16x16x32_bf16 v[46:49], v[176:179], v[196:199], v[46:49]
	v_mfma_f32_16x16x32_bf16 v[34:37], v[168:171], v[204:207], v[34:37]
	v_mfma_f32_16x16x32_bf16 v[38:41], v[176:179], v[204:207], v[38:41]
	v_mfma_f32_16x16x32_bf16 v[18:21], v[168:171], v[228:231], v[18:21]
	v_mfma_f32_16x16x32_bf16 v[22:25], v[176:179], v[228:231], v[22:25]
	v_mfma_f32_16x16x32_bf16 v[66:69], v[172:175], v[188:191], v[66:69]
	v_mfma_f32_16x16x32_bf16 v[70:73], v[180:183], v[188:191], v[70:73]
	v_mfma_f32_16x16x32_bf16 v[42:45], v[172:175], v[200:203], v[42:45]
	v_mfma_f32_16x16x32_bf16 v[46:49], v[180:183], v[200:203], v[46:49]
	v_mfma_f32_16x16x32_bf16 v[34:37], v[172:175], v[208:211], v[34:37]
	v_mfma_f32_16x16x32_bf16 v[38:41], v[180:183], v[208:211], v[38:41]
	v_mfma_f32_16x16x32_bf16 v[18:21], v[172:175], v[232:235], v[18:21]
	v_mfma_f32_16x16x32_bf16 v[22:25], v[180:183], v[232:235], v[22:25]
	s_barrier
	s_add_i32 s28, 0, 0x18000
	v_add_u32_e32 v146, s28, v147
	s_add_i32 s29, 0, 0x1c000
	ds_read_b128 v[152:155], v146
	ds_read_b128 v[156:159], v146 offset:1024
	ds_read_b128 v[160:163], v146 offset:2048
	ds_read_b128 v[164:167], v146 offset:3072
	v_add_u32_e32 v146, s29, v147
	ds_read_b128 v[168:171], v146
	ds_read_b128 v[172:175], v146 offset:1024
	ds_read_b128 v[176:179], v146 offset:2048
	ds_read_b128 v[180:183], v146 offset:3072
	s_mov_b32 m0, s22
	v_lshl_add_u64 v[224:225], s[48:49], 0, v[138:139]
	ds_read_b128 v[184:187], v151 offset:32768
	ds_read_b128 v[188:191], v151 offset:33792
	ds_read_b128 v[196:199], v151 offset:34816
	ds_read_b128 v[200:203], v151 offset:35840
	ds_read_b128 v[204:207], v151 offset:36864
	ds_read_b128 v[208:211], v151 offset:37888
	ds_read_b128 v[228:231], v151 offset:38912
	ds_read_b128 v[232:235], v151 offset:39936
	global_load_lds_dwordx4 v[224:225], off
	v_lshl_add_u64 v[224:225], s[48:49], 0, v[140:141]
	s_mov_b32 m0, s23
	s_nop 0
	global_load_lds_dwordx4 v[224:225], off
	s_waitcnt vmcnt(8)
	s_waitcnt lgkmcnt(0)
	s_barrier
	v_mfma_f32_16x16x32_bf16 v[126:129], v[152:155], v[184:187], v[126:129]
	v_mfma_f32_16x16x32_bf16 v[122:125], v[160:163], v[184:187], v[122:125]
	v_mfma_f32_16x16x32_bf16 v[110:113], v[152:155], v[196:199], v[110:113]
	v_mfma_f32_16x16x32_bf16 v[106:109], v[160:163], v[196:199], v[106:109]
	v_mfma_f32_16x16x32_bf16 v[94:97], v[152:155], v[204:207], v[94:97]
	v_mfma_f32_16x16x32_bf16 v[90:93], v[160:163], v[204:207], v[90:93]
	v_mfma_f32_16x16x32_bf16 v[82:85], v[152:155], v[228:231], v[82:85]
	v_mfma_f32_16x16x32_bf16 v[74:77], v[160:163], v[228:231], v[74:77]
	v_mfma_f32_16x16x32_bf16 v[126:129], v[156:159], v[188:191], v[126:129]
	v_mfma_f32_16x16x32_bf16 v[122:125], v[164:167], v[188:191], v[122:125]
	v_mfma_f32_16x16x32_bf16 v[110:113], v[156:159], v[200:203], v[110:113]
	v_mfma_f32_16x16x32_bf16 v[106:109], v[164:167], v[200:203], v[106:109]
	v_mfma_f32_16x16x32_bf16 v[94:97], v[156:159], v[208:211], v[94:97]
	v_mfma_f32_16x16x32_bf16 v[90:93], v[164:167], v[208:211], v[90:93]
	v_mfma_f32_16x16x32_bf16 v[82:85], v[156:159], v[232:235], v[82:85]
	v_mfma_f32_16x16x32_bf16 v[74:77], v[164:167], v[232:235], v[74:77]
	v_mfma_f32_16x16x32_bf16 v[118:121], v[168:171], v[184:187], v[118:121]
	v_mfma_f32_16x16x32_bf16 v[114:117], v[176:179], v[184:187], v[114:117]
	v_mfma_f32_16x16x32_bf16 v[102:105], v[168:171], v[196:199], v[102:105]
	v_mfma_f32_16x16x32_bf16 v[98:101], v[176:179], v[196:199], v[98:101]
	v_mfma_f32_16x16x32_bf16 v[86:89], v[168:171], v[204:207], v[86:89]
	v_mfma_f32_16x16x32_bf16 v[78:81], v[176:179], v[204:207], v[78:81]
	v_mfma_f32_16x16x32_bf16 v[62:65], v[168:171], v[228:231], v[62:65]
	v_mfma_f32_16x16x32_bf16 v[58:61], v[176:179], v[228:231], v[58:61]
	v_mfma_f32_16x16x32_bf16 v[118:121], v[172:175], v[188:191], v[118:121]
	v_mfma_f32_16x16x32_bf16 v[114:117], v[180:183], v[188:191], v[114:117]
	v_mfma_f32_16x16x32_bf16 v[102:105], v[172:175], v[200:203], v[102:105]
	v_mfma_f32_16x16x32_bf16 v[98:101], v[180:183], v[200:203], v[98:101]
	v_mfma_f32_16x16x32_bf16 v[86:89], v[172:175], v[208:211], v[86:89]
	v_mfma_f32_16x16x32_bf16 v[78:81], v[180:183], v[208:211], v[78:81]
	v_mfma_f32_16x16x32_bf16 v[62:65], v[172:175], v[232:235], v[62:65]
	v_mfma_f32_16x16x32_bf16 v[58:61], v[180:183], v[232:235], v[58:61]
	s_barrier
; #define PG8_STAGE(bufoff, gbase, voff) do { _Pragma("unroll") for (int _i = 0; _i < 2; ++_i) \
;         __builtin_amdgcn_global_load_lds((const unsigned*)((const char*)(gbase) + (voff)[_i]), (LAS unsigned*)(lds + (bufoff) + ldsw + _i * 8192), 16, 0, 0); } while (0)
; #define PG8_LDA(dst, b, h) do { _Pragma("unroll") for (int m = 0; m < 4; ++m) _Pragma("unroll") for (int k = 0; k < 2; ++k) dst[m][k] = *(const LAS bf16x8*)(lds + PG8_SA(b, h) + aoff + m * 2048 + k * 1024); } while (0)
; #define PG8_MMA(ai, bj, At, Bt) do { __builtin_amdgcn_s_setprio(1); _Pragma("unroll") for (int m = 0; m < 4; ++m) _Pragma("unroll") for (int n = 0; n < 2; ++n) _Pragma("unroll") for (int k = 0; k < 2; ++k) \
;         acc[ai][bj][m][n] = __builtin_amdgcn_mfma_f32_16x16x32_bf16(Bt[n][k], At[m][k], acc[ai][bj][m][n], 0, 0, 0); __builtin_amdgcn_s_setprio(0); } while (0)
; #define PG8_WAIT_V(n) asm volatile("s_waitcnt vmcnt(" #n ")" ::: "memory")
; #define PG8_WAIT_L(n) asm volatile("s_waitcnt lgkmcnt(" #n ")" ::: "memory")
; #define PG8_BAR __builtin_amdgcn_s_barrier()
; #define PG8_SCHED __builtin_amdgcn_sched_barrier(0)
; template <class Epi, class Sched, bool GATHER = false>
; __device__ __forceinline__ void gemm_phase(LAS unsigned char* lds, const int lda, const int ldb, const int K, const Sched& S, const Epi& E, const int* gidx = nullptr) {
;     ...
;             PG8_LDA(At, 1, 1); PG8_STAGE(PG8_SB(1, 0), b3, voffB); PG8_STAGE(PG8_SB(1, 1), b3 + hstepB, voffB); PG8_STAGE(PG8_SA(1, 0), a3, o2[0]);
;             PG8_WAIT_V(8); PG8_WAIT_L(0); PG8_BAR; PG8_MMA(1, 0, At, B0); PG8_MMA(1, 1, At, B1); PG8_BAR; PG8_SCHED;
;         }
;         if (wr == 0) PG8_BAR;
	s_add_i32 s28, s28, s9
	v_lshl_add_u64 v[148:149], v[148:149], 0, s[64:65]
	s_mov_b32 m0, s28
	ds_read_b128 v[184:187], v151 offset:49152
	ds_read_b128 v[188:191], v151 offset:50176
	ds_read_b128 v[196:199], v151 offset:51200
	ds_read_b128 v[200:203], v151 offset:52224
	ds_read_b128 v[204:207], v151 offset:53248
	ds_read_b128 v[208:211], v151 offset:54272
	ds_read_b128 v[228:231], v151 offset:55296
	ds_read_b128 v[232:235], v151 offset:56320
	global_load_lds_dwordx4 v[148:149], off
	s_add_i32 m0, s28, 0x2000
	s_add_u32 s12, s12, 0x40080
	v_lshl_add_u64 v[148:149], v[192:193], 0, s[64:65]
	s_addc_u32 s13, s13, 0
	s_add_i32 s28, s29, s9
	global_load_lds_dwordx4 v[148:149], off
	v_lshl_add_u64 v[148:149], s[12:13], 0, v[132:133]
	s_mov_b32 m0, s28
	s_nop 0
	global_load_lds_dwordx4 v[148:149], off
	v_lshl_add_u64 v[148:149], s[12:13], 0, v[130:131]
	s_add_i32 m0, s28, 0x2000
	s_nop 0
	global_load_lds_dwordx4 v[148:149], off
	v_lshl_add_u64 v[148:149], v[214:215], 0, s[64:65]
	s_mov_b32 m0, s50
	s_nop 0
	global_load_lds_dwordx4 v[148:149], off
	v_lshl_add_u64 v[148:149], v[222:223], 0, s[64:65]
	s_mov_b32 m0, s51
	s_nop 0
	global_load_lds_dwordx4 v[148:149], off
	s_waitcnt vmcnt(8)
	s_waitcnt lgkmcnt(0)
	s_barrier
	v_mfma_f32_16x16x32_bf16 v[54:57], v[152:155], v[184:187], v[54:57]
	v_mfma_f32_16x16x32_bf16 v[50:53], v[160:163], v[184:187], v[50:53]
	v_mfma_f32_16x16x32_bf16 v[30:33], v[152:155], v[196:199], v[30:33]
	v_mfma_f32_16x16x32_bf16 v[26:29], v[160:163], v[196:199], v[26:29]
	v_mfma_f32_16x16x32_bf16 v[14:17], v[152:155], v[204:207], v[14:17]
	v_mfma_f32_16x16x32_bf16 v[10:13], v[160:163], v[204:207], v[10:13]
	v_mfma_f32_16x16x32_bf16 v[6:9], v[152:155], v[228:231], v[6:9]
	v_mfma_f32_16x16x32_bf16 v[2:5], v[160:163], v[228:231], v[2:5]
	v_mfma_f32_16x16x32_bf16 v[54:57], v[156:159], v[188:191], v[54:57]
	v_mfma_f32_16x16x32_bf16 v[50:53], v[164:167], v[188:191], v[50:53]
	v_mfma_f32_16x16x32_bf16 v[30:33], v[156:159], v[200:203], v[30:33]
	v_mfma_f32_16x16x32_bf16 v[26:29], v[164:167], v[200:203], v[26:29]
	v_mfma_f32_16x16x32_bf16 v[14:17], v[156:159], v[208:211], v[14:17]
	v_mfma_f32_16x16x32_bf16 v[10:13], v[164:167], v[208:211], v[10:13]
	v_mfma_f32_16x16x32_bf16 v[6:9], v[156:159], v[232:235], v[6:9]
	v_mfma_f32_16x16x32_bf16 v[2:5], v[164:167], v[232:235], v[2:5]
	v_mfma_f32_16x16x32_bf16 v[66:69], v[168:171], v[184:187], v[66:69]
	v_mfma_f32_16x16x32_bf16 v[70:73], v[176:179], v[184:187], v[70:73]
	v_mfma_f32_16x16x32_bf16 v[42:45], v[168:171], v[196:199], v[42:45]
	v_mfma_f32_16x16x32_bf16 v[46:49], v[176:179], v[196:199], v[46:49]
	v_mfma_f32_16x16x32_bf16 v[34:37], v[168:171], v[204:207], v[34:37]
	v_mfma_f32_16x16x32_bf16 v[38:41], v[176:179], v[204:207], v[38:41]
	v_mfma_f32_16x16x32_bf16 v[18:21], v[168:171], v[228:231], v[18:21]
	v_mfma_f32_16x16x32_bf16 v[22:25], v[176:179], v[228:231], v[22:25]
	v_mfma_f32_16x16x32_bf16 v[66:69], v[172:175], v[188:191], v[66:69]
	v_mfma_f32_16x16x32_bf16 v[70:73], v[180:183], v[188:191], v[70:73]
	v_mfma_f32_16x16x32_bf16 v[42:45], v[172:175], v[200:203], v[42:45]
	v_mfma_f32_16x16x32_bf16 v[46:49], v[180:183], v[200:203], v[46:49]
	v_mfma_f32_16x16x32_bf16 v[34:37], v[172:175], v[208:211], v[34:37]
	v_mfma_f32_16x16x32_bf16 v[38:41], v[180:183], v[208:211], v[38:41]
	v_mfma_f32_16x16x32_bf16 v[18:21], v[172:175], v[232:235], v[18:21]
	v_mfma_f32_16x16x32_bf16 v[22:25], v[180:183], v[232:235], v[22:25]
	s_barrier
	s_add_i32 s72, s72, 2
	s_add_u32 s44, s44, 0x100
	s_addc_u32 s45, s45, 0
	s_add_u32 s70, s70, 0x100
	s_addc_u32 s71, s71, 0
	s_cmp_gt_u32 s72, 13
	s_cbranch_scc0 .LBB0_1733
	s_and_b64 vcc, exec, s[36:37]
	s_cbranch_vccz .LBB0_1736
	s_barrier
